# v33 + write-through (sc1) row stores in pool_diff, LayerNorm phases, gather and final combine
# baseline (speedup 1.0000x reference)
.Lpd_pre_summed:
	s_waitcnt vmcnt(31)
	v_pk_add_f32 v[168:169], v[168:169], v[40:41]
	v_pk_add_f32 v[170:171], v[170:171], v[42:43]
	s_cmp_lt_u32 1, s74
	s_cselect_b32 s76, 0x3f800000, s75
	v_fma_f32 v172, s76, v168, -v40
	v_fma_f32 v173, s76, v169, -v41
	v_fma_f32 v174, s76, v170, -v42
	v_fma_f32 v175, s76, v171, -v43
	v_cvt_pk_bf16_f32 v176, v172, v173
	v_cvt_pk_bf16_f32 v177, v174, v175
	s_add_i32 s100, s73, 0
	s_lshl_b32 s98, s100, 12
	v_lshl_add_u64 v[178:179], v[2:3], 0, s[98:99]
	global_store_dwordx2 v[178:179], v[176:177], off sc1
	s_add_i32 s76, s73, 16
	s_lshl_b32 s98, s76, 13
	v_lshl_add_u64 v[178:179], v[0:1], 0, s[98:99]
	global_load_dwordx4 v[40:43], v[178:179], off
	s_cmp_lt_u32 1, s74
	s_cbranch_scc1 .Lpd_keep_0
	s_waitcnt vmcnt(32)
	v_sub_f32_e32 v168, v168, v104
	v_sub_f32_e32 v169, v169, v105
	v_sub_f32_e32 v170, v170, v106
	v_sub_f32_e32 v171, v171, v107
.Lpd_keep_0:
	s_add_i32 s76, s73, 17
	s_sub_i32 s76, s76, s43
	s_max_i32 s76, s76, s42
	s_lshl_b32 s98, s76, 13
	v_lshl_add_u64 v[178:179], v[0:1], 0, s[98:99]
	global_load_dwordx4 v[104:107], v[178:179], off
	s_waitcnt vmcnt(32)
	v_pk_add_f32 v[168:169], v[168:169], v[44:45]
	v_pk_add_f32 v[170:171], v[170:171], v[46:47]
	s_cmp_lt_u32 2, s74
	s_cselect_b32 s76, 0x3f000000, s75
	v_fma_f32 v172, s76, v168, -v44
	v_fma_f32 v173, s76, v169, -v45
	v_fma_f32 v174, s76, v170, -v46
	v_fma_f32 v175, s76, v171, -v47
	v_cvt_pk_bf16_f32 v176, v172, v173
	v_cvt_pk_bf16_f32 v177, v174, v175
	s_add_i32 s100, s73, 1
	s_lshl_b32 s98, s100, 12
	v_lshl_add_u64 v[178:179], v[2:3], 0, s[98:99]
	global_store_dwordx2 v[178:179], v[176:177], off sc1
	s_add_i32 s76, s73, 17
	s_lshl_b32 s98, s76, 13
	v_lshl_add_u64 v[178:179], v[0:1], 0, s[98:99]
	global_load_dwordx4 v[44:47], v[178:179], off
	s_cmp_lt_u32 2, s74
	s_cbranch_scc1 .Lpd_keep_1
	s_waitcnt vmcnt(33)
	v_sub_f32_e32 v168, v168, v108
	v_sub_f32_e32 v169, v169, v109
	v_sub_f32_e32 v170, v170, v110
	v_sub_f32_e32 v171, v171, v111
.Lpd_keep_1:
	s_add_i32 s76, s73, 18
	s_sub_i32 s76, s76, s43
	s_max_i32 s76, s76, s42
	s_lshl_b32 s98, s76, 13
	v_lshl_add_u64 v[178:179], v[0:1], 0, s[98:99]
	global_load_dwordx4 v[108:111], v[178:179], off
	s_waitcnt vmcnt(33)
	v_pk_add_f32 v[168:169], v[168:169], v[48:49]
	v_pk_add_f32 v[170:171], v[170:171], v[50:51]
	s_cmp_lt_u32 3, s74
	s_cselect_b32 s76, 0x3eaaaaab, s75
	v_fma_f32 v172, s76, v168, -v48
	v_fma_f32 v173, s76, v169, -v49
	v_fma_f32 v174, s76, v170, -v50
	v_fma_f32 v175, s76, v171, -v51
	v_cvt_pk_bf16_f32 v176, v172, v173
	v_cvt_pk_bf16_f32 v177, v174, v175
	s_add_i32 s100, s73, 2
	s_lshl_b32 s98, s100, 12
	v_lshl_add_u64 v[178:179], v[2:3], 0, s[98:99]
	global_store_dwordx2 v[178:179], v[176:177], off sc1
	s_add_i32 s76, s73, 18
	s_lshl_b32 s98, s76, 13
	v_lshl_add_u64 v[178:179], v[0:1], 0, s[98:99]
	global_load_dwordx4 v[48:51], v[178:179], off
	s_cmp_lt_u32 3, s74
	s_cbranch_scc1 .Lpd_keep_2
	s_waitcnt vmcnt(34)
	v_sub_f32_e32 v168, v168, v112
	v_sub_f32_e32 v169, v169, v113
	v_sub_f32_e32 v170, v170, v114
	v_sub_f32_e32 v171, v171, v115
.Lpd_keep_2:
	s_add_i32 s76, s73, 19
	s_sub_i32 s76, s76, s43
	s_max_i32 s76, s76, s42
	s_lshl_b32 s98, s76, 13
	v_lshl_add_u64 v[178:179], v[0:1], 0, s[98:99]
	global_load_dwordx4 v[112:115], v[178:179], off
	s_waitcnt vmcnt(34)
	v_pk_add_f32 v[168:169], v[168:169], v[52:53]
	v_pk_add_f32 v[170:171], v[170:171], v[54:55]
	s_cmp_lt_u32 4, s74
	s_cselect_b32 s76, 0x3e800000, s75
	v_fma_f32 v172, s76, v168, -v52
	v_fma_f32 v173, s76, v169, -v53
	v_fma_f32 v174, s76, v170, -v54
	v_fma_f32 v175, s76, v171, -v55
	v_cvt_pk_bf16_f32 v176, v172, v173
	v_cvt_pk_bf16_f32 v177, v174, v175
	s_add_i32 s100, s73, 3
	s_lshl_b32 s98, s100, 12
	v_lshl_add_u64 v[178:179], v[2:3], 0, s[98:99]
	global_store_dwordx2 v[178:179], v[176:177], off sc1
	s_add_i32 s76, s73, 19
	s_lshl_b32 s98, s76, 13
	v_lshl_add_u64 v[178:179], v[0:1], 0, s[98:99]
	global_load_dwordx4 v[52:55], v[178:179], off
	s_cmp_lt_u32 4, s74
	s_cbranch_scc1 .Lpd_keep_3
	s_waitcnt vmcnt(35)
	v_sub_f32_e32 v168, v168, v116
	v_sub_f32_e32 v169, v169, v117
	v_sub_f32_e32 v170, v170, v118
	v_sub_f32_e32 v171, v171, v119
.Lpd_keep_3:
	s_add_i32 s76, s73, 20
	s_sub_i32 s76, s76, s43
	s_max_i32 s76, s76, s42
	s_lshl_b32 s98, s76, 13
	v_lshl_add_u64 v[178:179], v[0:1], 0, s[98:99]
	global_load_dwordx4 v[116:119], v[178:179], off
	s_waitcnt vmcnt(35)
	v_pk_add_f32 v[168:169], v[168:169], v[56:57]
	v_pk_add_f32 v[170:171], v[170:171], v[58:59]
	s_cmp_lt_u32 5, s74
	s_cselect_b32 s76, 0x3e4ccccd, s75
	v_fma_f32 v172, s76, v168, -v56
	v_fma_f32 v173, s76, v169, -v57
	v_fma_f32 v174, s76, v170, -v58
	v_fma_f32 v175, s76, v171, -v59
	v_cvt_pk_bf16_f32 v176, v172, v173
	v_cvt_pk_bf16_f32 v177, v174, v175
	s_add_i32 s100, s73, 4
	s_lshl_b32 s98, s100, 12
	v_lshl_add_u64 v[178:179], v[2:3], 0, s[98:99]
	global_store_dwordx2 v[178:179], v[176:177], off sc1
	s_add_i32 s76, s73, 20
	s_lshl_b32 s98, s76, 13
	v_lshl_add_u64 v[178:179], v[0:1], 0, s[98:99]
	global_load_dwordx4 v[56:59], v[178:179], off
	s_cmp_lt_u32 5, s74
	s_cbranch_scc1 .Lpd_keep_4
	s_waitcnt vmcnt(36)
	v_sub_f32_e32 v168, v168, v120
	v_sub_f32_e32 v169, v169, v121
	v_sub_f32_e32 v170, v170, v122
	v_sub_f32_e32 v171, v171, v123
.Lpd_keep_4:
	s_add_i32 s76, s73, 21
	s_sub_i32 s76, s76, s43
	s_max_i32 s76, s76, s42
	s_lshl_b32 s98, s76, 13
	v_lshl_add_u64 v[178:179], v[0:1], 0, s[98:99]
	global_load_dwordx4 v[120:123], v[178:179], off
	s_waitcnt vmcnt(36)
	v_pk_add_f32 v[168:169], v[168:169], v[60:61]
	v_pk_add_f32 v[170:171], v[170:171], v[62:63]
	s_cmp_lt_u32 6, s74
	s_cselect_b32 s76, 0x3e2aaaab, s75
	v_fma_f32 v172, s76, v168, -v60
	v_fma_f32 v173, s76, v169, -v61
	v_fma_f32 v174, s76, v170, -v62
	v_fma_f32 v175, s76, v171, -v63
	v_cvt_pk_bf16_f32 v176, v172, v173
	v_cvt_pk_bf16_f32 v177, v174, v175
	s_add_i32 s100, s73, 5
	s_lshl_b32 s98, s100, 12
	v_lshl_add_u64 v[178:179], v[2:3], 0, s[98:99]
	global_store_dwordx2 v[178:179], v[176:177], off sc1
	s_add_i32 s76, s73, 21
	s_lshl_b32 s98, s76, 13
	v_lshl_add_u64 v[178:179], v[0:1], 0, s[98:99]
	global_load_dwordx4 v[60:63], v[178:179], off
	s_cmp_lt_u32 6, s74
	s_cbranch_scc1 .Lpd_keep_5
	s_waitcnt vmcnt(37)
	v_sub_f32_e32 v168, v168, v124
	v_sub_f32_e32 v169, v169, v125
	v_sub_f32_e32 v170, v170, v126
	v_sub_f32_e32 v171, v171, v127
.Lpd_keep_5:
	s_add_i32 s76, s73, 22
	s_sub_i32 s76, s76, s43
	s_max_i32 s76, s76, s42
	s_lshl_b32 s98, s76, 13
	v_lshl_add_u64 v[178:179], v[0:1], 0, s[98:99]
	global_load_dwordx4 v[124:127], v[178:179], off
	s_waitcnt vmcnt(37)
	v_pk_add_f32 v[168:169], v[168:169], v[64:65]
	v_pk_add_f32 v[170:171], v[170:171], v[66:67]
	s_cmp_lt_u32 7, s74
	s_cselect_b32 s76, 0x3e124925, s75
	v_fma_f32 v172, s76, v168, -v64
	v_fma_f32 v173, s76, v169, -v65
	v_fma_f32 v174, s76, v170, -v66
	v_fma_f32 v175, s76, v171, -v67
	v_cvt_pk_bf16_f32 v176, v172, v173
	v_cvt_pk_bf16_f32 v177, v174, v175
	s_add_i32 s100, s73, 6
	s_lshl_b32 s98, s100, 12
	v_lshl_add_u64 v[178:179], v[2:3], 0, s[98:99]
	global_store_dwordx2 v[178:179], v[176:177], off sc1
	s_add_i32 s76, s73, 22
	s_lshl_b32 s98, s76, 13
	v_lshl_add_u64 v[178:179], v[0:1], 0, s[98:99]
	global_load_dwordx4 v[64:67], v[178:179], off
	s_cmp_lt_u32 7, s74
	s_cbranch_scc1 .Lpd_keep_6
	s_waitcnt vmcnt(38)
	v_sub_f32_e32 v168, v168, v128
	v_sub_f32_e32 v169, v169, v129
	v_sub_f32_e32 v170, v170, v130
	v_sub_f32_e32 v171, v171, v131
.Lpd_keep_6:
	s_add_i32 s76, s73, 23
	s_sub_i32 s76, s76, s43
	s_max_i32 s76, s76, s42
	s_lshl_b32 s98, s76, 13
	v_lshl_add_u64 v[178:179], v[0:1], 0, s[98:99]
	global_load_dwordx4 v[128:131], v[178:179], off
	s_waitcnt vmcnt(38)
	v_pk_add_f32 v[168:169], v[168:169], v[68:69]
	v_pk_add_f32 v[170:171], v[170:171], v[70:71]
	s_cmp_lt_u32 8, s74
	s_cselect_b32 s76, 0x3e000000, s75
	v_fma_f32 v172, s76, v168, -v68
	v_fma_f32 v173, s76, v169, -v69
	v_fma_f32 v174, s76, v170, -v70
	v_fma_f32 v175, s76, v171, -v71
	v_cvt_pk_bf16_f32 v176, v172, v173
	v_cvt_pk_bf16_f32 v177, v174, v175
	s_add_i32 s100, s73, 7
	s_lshl_b32 s98, s100, 12
	v_lshl_add_u64 v[178:179], v[2:3], 0, s[98:99]
	global_store_dwordx2 v[178:179], v[176:177], off sc1
	s_add_i32 s76, s73, 23
	s_lshl_b32 s98, s76, 13
	v_lshl_add_u64 v[178:179], v[0:1], 0, s[98:99]
	global_load_dwordx4 v[68:71], v[178:179], off
	s_cmp_lt_u32 8, s74
	s_cbranch_scc1 .Lpd_keep_7
	s_waitcnt vmcnt(39)
	v_sub_f32_e32 v168, v168, v132
	v_sub_f32_e32 v169, v169, v133
	v_sub_f32_e32 v170, v170, v134
	v_sub_f32_e32 v171, v171, v135
.Lpd_keep_7:
	s_add_i32 s76, s73, 24
	s_sub_i32 s76, s76, s43
	s_max_i32 s76, s76, s42
	s_lshl_b32 s98, s76, 13
	v_lshl_add_u64 v[178:179], v[0:1], 0, s[98:99]
	global_load_dwordx4 v[132:135], v[178:179], off
	s_waitcnt vmcnt(39)
	v_pk_add_f32 v[168:169], v[168:169], v[72:73]
	v_pk_add_f32 v[170:171], v[170:171], v[74:75]
	s_cmp_lt_u32 9, s74
	s_cselect_b32 s76, 0x3de38e39, s75
	v_fma_f32 v172, s76, v168, -v72
	v_fma_f32 v173, s76, v169, -v73
	v_fma_f32 v174, s76, v170, -v74
	v_fma_f32 v175, s76, v171, -v75
	v_cvt_pk_bf16_f32 v176, v172, v173
	v_cvt_pk_bf16_f32 v177, v174, v175
	s_add_i32 s100, s73, 8
	s_lshl_b32 s98, s100, 12
	v_lshl_add_u64 v[178:179], v[2:3], 0, s[98:99]
	global_store_dwordx2 v[178:179], v[176:177], off sc1
	s_add_i32 s76, s73, 24
	s_lshl_b32 s98, s76, 13
	v_lshl_add_u64 v[178:179], v[0:1], 0, s[98:99]
	global_load_dwordx4 v[72:75], v[178:179], off
	s_cmp_lt_u32 9, s74
	s_cbranch_scc1 .Lpd_keep_8
	s_waitcnt vmcnt(40)
	v_sub_f32_e32 v168, v168, v136
	v_sub_f32_e32 v169, v169, v137
	v_sub_f32_e32 v170, v170, v138
	v_sub_f32_e32 v171, v171, v139
.Lpd_keep_8:
	s_add_i32 s76, s73, 25
	s_sub_i32 s76, s76, s43
	s_max_i32 s76, s76, s42
	s_lshl_b32 s98, s76, 13
	v_lshl_add_u64 v[178:179], v[0:1], 0, s[98:99]
	global_load_dwordx4 v[136:139], v[178:179], off
	s_waitcnt vmcnt(40)
	v_pk_add_f32 v[168:169], v[168:169], v[76:77]
	v_pk_add_f32 v[170:171], v[170:171], v[78:79]
	s_cmp_lt_u32 10, s74
	s_cselect_b32 s76, 0x3dcccccd, s75
	v_fma_f32 v172, s76, v168, -v76
	v_fma_f32 v173, s76, v169, -v77
	v_fma_f32 v174, s76, v170, -v78
	v_fma_f32 v175, s76, v171, -v79
	v_cvt_pk_bf16_f32 v176, v172, v173
	v_cvt_pk_bf16_f32 v177, v174, v175
	s_add_i32 s100, s73, 9
	s_lshl_b32 s98, s100, 12
	v_lshl_add_u64 v[178:179], v[2:3], 0, s[98:99]
	global_store_dwordx2 v[178:179], v[176:177], off sc1
	s_add_i32 s76, s73, 25
	s_lshl_b32 s98, s76, 13
	v_lshl_add_u64 v[178:179], v[0:1], 0, s[98:99]
	global_load_dwordx4 v[76:79], v[178:179], off
	s_cmp_lt_u32 10, s74
	s_cbranch_scc1 .Lpd_keep_9
	s_waitcnt vmcnt(41)
	v_sub_f32_e32 v168, v168, v140
	v_sub_f32_e32 v169, v169, v141
	v_sub_f32_e32 v170, v170, v142
	v_sub_f32_e32 v171, v171, v143
.Lpd_keep_9:
	s_add_i32 s76, s73, 26
	s_sub_i32 s76, s76, s43
	s_max_i32 s76, s76, s42
	s_lshl_b32 s98, s76, 13
	v_lshl_add_u64 v[178:179], v[0:1], 0, s[98:99]
	global_load_dwordx4 v[140:143], v[178:179], off
	s_waitcnt vmcnt(41)
	v_pk_add_f32 v[168:169], v[168:169], v[80:81]
	v_pk_add_f32 v[170:171], v[170:171], v[82:83]
	s_cmp_lt_u32 11, s74
	s_cselect_b32 s76, 0x3dba2e8c, s75
	v_fma_f32 v172, s76, v168, -v80
	v_fma_f32 v173, s76, v169, -v81
	v_fma_f32 v174, s76, v170, -v82
	v_fma_f32 v175, s76, v171, -v83
	v_cvt_pk_bf16_f32 v176, v172, v173
	v_cvt_pk_bf16_f32 v177, v174, v175
	s_add_i32 s100, s73, 10
	s_lshl_b32 s98, s100, 12
	v_lshl_add_u64 v[178:179], v[2:3], 0, s[98:99]
	global_store_dwordx2 v[178:179], v[176:177], off sc1
	s_add_i32 s76, s73, 26
	s_lshl_b32 s98, s76, 13
	v_lshl_add_u64 v[178:179], v[0:1], 0, s[98:99]
	global_load_dwordx4 v[80:83], v[178:179], off
	s_cmp_lt_u32 11, s74
	s_cbranch_scc1 .Lpd_keep_10
	s_waitcnt vmcnt(42)
	v_sub_f32_e32 v168, v168, v144
	v_sub_f32_e32 v169, v169, v145
	v_sub_f32_e32 v170, v170, v146
	v_sub_f32_e32 v171, v171, v147
.Lpd_keep_10:
	s_add_i32 s76, s73, 27
	s_sub_i32 s76, s76, s43
	s_max_i32 s76, s76, s42
	s_lshl_b32 s98, s76, 13
	v_lshl_add_u64 v[178:179], v[0:1], 0, s[98:99]
	global_load_dwordx4 v[144:147], v[178:179], off
	s_waitcnt vmcnt(42)
	v_pk_add_f32 v[168:169], v[168:169], v[84:85]
	v_pk_add_f32 v[170:171], v[170:171], v[86:87]
	s_cmp_lt_u32 12, s74
	s_cselect_b32 s76, 0x3daaaaab, s75
	v_fma_f32 v172, s76, v168, -v84
	v_fma_f32 v173, s76, v169, -v85
	v_fma_f32 v174, s76, v170, -v86
	v_fma_f32 v175, s76, v171, -v87
	v_cvt_pk_bf16_f32 v176, v172, v173
	v_cvt_pk_bf16_f32 v177, v174, v175
	s_add_i32 s100, s73, 11
	s_lshl_b32 s98, s100, 12
	v_lshl_add_u64 v[178:179], v[2:3], 0, s[98:99]
	global_store_dwordx2 v[178:179], v[176:177], off sc1
	s_add_i32 s76, s73, 27
	s_lshl_b32 s98, s76, 13
	v_lshl_add_u64 v[178:179], v[0:1], 0, s[98:99]
	global_load_dwordx4 v[84:87], v[178:179], off
	s_cmp_lt_u32 12, s74
	s_cbranch_scc1 .Lpd_keep_11
	s_waitcnt vmcnt(43)
	v_sub_f32_e32 v168, v168, v148
	v_sub_f32_e32 v169, v169, v149
	v_sub_f32_e32 v170, v170, v150
	v_sub_f32_e32 v171, v171, v151
.Lpd_keep_11:
	s_add_i32 s76, s73, 28
	s_sub_i32 s76, s76, s43
	s_max_i32 s76, s76, s42
	s_lshl_b32 s98, s76, 13
	v_lshl_add_u64 v[178:179], v[0:1], 0, s[98:99]
	global_load_dwordx4 v[148:151], v[178:179], off
	s_waitcnt vmcnt(43)
	v_pk_add_f32 v[168:169], v[168:169], v[88:89]
	v_pk_add_f32 v[170:171], v[170:171], v[90:91]
	s_cmp_lt_u32 13, s74
	s_cselect_b32 s76, 0x3d9d89d9, s75
	v_fma_f32 v172, s76, v168, -v88
	v_fma_f32 v173, s76, v169, -v89
	v_fma_f32 v174, s76, v170, -v90
	v_fma_f32 v175, s76, v171, -v91
	v_cvt_pk_bf16_f32 v176, v172, v173
	v_cvt_pk_bf16_f32 v177, v174, v175
	s_add_i32 s100, s73, 12
	s_lshl_b32 s98, s100, 12
	v_lshl_add_u64 v[178:179], v[2:3], 0, s[98:99]
	global_store_dwordx2 v[178:179], v[176:177], off sc1
	s_add_i32 s76, s73, 28
	s_lshl_b32 s98, s76, 13
	v_lshl_add_u64 v[178:179], v[0:1], 0, s[98:99]
	global_load_dwordx4 v[88:91], v[178:179], off
	s_cmp_lt_u32 13, s74
	s_cbranch_scc1 .Lpd_keep_12
	s_waitcnt vmcnt(44)
	v_sub_f32_e32 v168, v168, v152
	v_sub_f32_e32 v169, v169, v153
	v_sub_f32_e32 v170, v170, v154
	v_sub_f32_e32 v171, v171, v155
.Lpd_keep_12:
	s_add_i32 s76, s73, 29
	s_sub_i32 s76, s76, s43
	s_max_i32 s76, s76, s42
	s_lshl_b32 s98, s76, 13
	v_lshl_add_u64 v[178:179], v[0:1], 0, s[98:99]
	global_load_dwordx4 v[152:155], v[178:179], off
	s_waitcnt vmcnt(44)
	v_pk_add_f32 v[168:169], v[168:169], v[92:93]
	v_pk_add_f32 v[170:171], v[170:171], v[94:95]
	s_cmp_lt_u32 14, s74
	s_cselect_b32 s76, 0x3d924925, s75
	v_fma_f32 v172, s76, v168, -v92
	v_fma_f32 v173, s76, v169, -v93
	v_fma_f32 v174, s76, v170, -v94
	v_fma_f32 v175, s76, v171, -v95
	v_cvt_pk_bf16_f32 v176, v172, v173
	v_cvt_pk_bf16_f32 v177, v174, v175
	s_add_i32 s100, s73, 13
	s_lshl_b32 s98, s100, 12
	v_lshl_add_u64 v[178:179], v[2:3], 0, s[98:99]
	global_store_dwordx2 v[178:179], v[176:177], off sc1
	s_add_i32 s76, s73, 29
	s_lshl_b32 s98, s76, 13
	v_lshl_add_u64 v[178:179], v[0:1], 0, s[98:99]
	global_load_dwordx4 v[92:95], v[178:179], off
	s_cmp_lt_u32 14, s74
	s_cbranch_scc1 .Lpd_keep_13
	s_waitcnt vmcnt(45)
	v_sub_f32_e32 v168, v168, v156
	v_sub_f32_e32 v169, v169, v157
	v_sub_f32_e32 v170, v170, v158
	v_sub_f32_e32 v171, v171, v159
.Lpd_keep_13:
	s_add_i32 s76, s73, 30
	s_sub_i32 s76, s76, s43
	s_max_i32 s76, s76, s42
	s_lshl_b32 s98, s76, 13
	v_lshl_add_u64 v[178:179], v[0:1], 0, s[98:99]
	global_load_dwordx4 v[156:159], v[178:179], off
	s_waitcnt vmcnt(45)
	v_pk_add_f32 v[168:169], v[168:169], v[96:97]
	v_pk_add_f32 v[170:171], v[170:171], v[98:99]
	s_cmp_lt_u32 15, s74
	s_cselect_b32 s76, 0x3d888889, s75
	v_fma_f32 v172, s76, v168, -v96
	v_fma_f32 v173, s76, v169, -v97
	v_fma_f32 v174, s76, v170, -v98
	v_fma_f32 v175, s76, v171, -v99
	v_cvt_pk_bf16_f32 v176, v172, v173
	v_cvt_pk_bf16_f32 v177, v174, v175
	s_add_i32 s100, s73, 14
	s_lshl_b32 s98, s100, 12
	v_lshl_add_u64 v[178:179], v[2:3], 0, s[98:99]
	global_store_dwordx2 v[178:179], v[176:177], off sc1
	s_add_i32 s76, s73, 30
	s_lshl_b32 s98, s76, 13
	v_lshl_add_u64 v[178:179], v[0:1], 0, s[98:99]
	global_load_dwordx4 v[96:99], v[178:179], off
	s_cmp_lt_u32 15, s74
	s_cbranch_scc1 .Lpd_keep_14
	s_waitcnt vmcnt(46)
	v_sub_f32_e32 v168, v168, v160
	v_sub_f32_e32 v169, v169, v161
	v_sub_f32_e32 v170, v170, v162
	v_sub_f32_e32 v171, v171, v163
.Lpd_keep_14:
	s_add_i32 s76, s73, 31
	s_sub_i32 s76, s76, s43
	s_max_i32 s76, s76, s42
	s_lshl_b32 s98, s76, 13
	v_lshl_add_u64 v[178:179], v[0:1], 0, s[98:99]
	global_load_dwordx4 v[160:163], v[178:179], off
	s_waitcnt vmcnt(46)
	v_pk_add_f32 v[168:169], v[168:169], v[100:101]
	v_pk_add_f32 v[170:171], v[170:171], v[102:103]
	v_fma_f32 v172, s75, v168, -v100
	v_fma_f32 v173, s75, v169, -v101
	v_fma_f32 v174, s75, v170, -v102
	v_fma_f32 v175, s75, v171, -v103
	v_cvt_pk_bf16_f32 v176, v172, v173
	v_cvt_pk_bf16_f32 v177, v174, v175
	s_add_i32 s100, s73, 15
	s_lshl_b32 s98, s100, 12
	v_lshl_add_u64 v[178:179], v[2:3], 0, s[98:99]
	global_store_dwordx2 v[178:179], v[176:177], off sc1
	s_add_i32 s76, s73, 31
	s_lshl_b32 s98, s76, 13
	v_lshl_add_u64 v[178:179], v[0:1], 0, s[98:99]
	global_load_dwordx4 v[100:103], v[178:179], off
	s_waitcnt vmcnt(47)
	v_sub_f32_e32 v168, v168, v164
	v_sub_f32_e32 v169, v169, v165
	v_sub_f32_e32 v170, v170, v166
	v_sub_f32_e32 v171, v171, v167
	s_waitcnt vmcnt(45)
	v_pk_add_f32 v[168:169], v[168:169], v[40:41]
	v_pk_add_f32 v[170:171], v[170:171], v[42:43]
	v_fma_f32 v172, s75, v168, -v40
	v_fma_f32 v173, s75, v169, -v41
	v_fma_f32 v174, s75, v170, -v42
	v_fma_f32 v175, s75, v171, -v43
	v_cvt_pk_bf16_f32 v176, v172, v173
	v_cvt_pk_bf16_f32 v177, v174, v175
	s_add_i32 s100, s73, 16
	s_lshl_b32 s98, s100, 12
	v_lshl_add_u64 v[178:179], v[2:3], 0, s[98:99]
	global_store_dwordx2 v[178:179], v[176:177], off sc1
	s_waitcnt vmcnt(45)
	v_sub_f32_e32 v168, v168, v104
	v_sub_f32_e32 v169, v169, v105
	v_sub_f32_e32 v170, v170, v106
	v_sub_f32_e32 v171, v171, v107
	s_waitcnt vmcnt(43)
	v_pk_add_f32 v[168:169], v[168:169], v[44:45]
	v_pk_add_f32 v[170:171], v[170:171], v[46:47]
	v_fma_f32 v172, s75, v168, -v44
	v_fma_f32 v173, s75, v169, -v45
	v_fma_f32 v174, s75, v170, -v46
	v_fma_f32 v175, s75, v171, -v47
	v_cvt_pk_bf16_f32 v176, v172, v173
	v_cvt_pk_bf16_f32 v177, v174, v175
	s_add_i32 s100, s73, 17
	s_lshl_b32 s98, s100, 12
	v_lshl_add_u64 v[178:179], v[2:3], 0, s[98:99]
	global_store_dwordx2 v[178:179], v[176:177], off sc1
	s_waitcnt vmcnt(43)
	v_sub_f32_e32 v168, v168, v108
	v_sub_f32_e32 v169, v169, v109
	v_sub_f32_e32 v170, v170, v110
	v_sub_f32_e32 v171, v171, v111
	s_waitcnt vmcnt(41)
	v_pk_add_f32 v[168:169], v[168:169], v[48:49]
	v_pk_add_f32 v[170:171], v[170:171], v[50:51]
	v_fma_f32 v172, s75, v168, -v48
	v_fma_f32 v173, s75, v169, -v49
	v_fma_f32 v174, s75, v170, -v50
	v_fma_f32 v175, s75, v171, -v51
	v_cvt_pk_bf16_f32 v176, v172, v173
	v_cvt_pk_bf16_f32 v177, v174, v175
	s_add_i32 s100, s73, 18
	s_lshl_b32 s98, s100, 12
	v_lshl_add_u64 v[178:179], v[2:3], 0, s[98:99]
	global_store_dwordx2 v[178:179], v[176:177], off sc1
	s_waitcnt vmcnt(41)
	v_sub_f32_e32 v168, v168, v112
	v_sub_f32_e32 v169, v169, v113
	v_sub_f32_e32 v170, v170, v114
	v_sub_f32_e32 v171, v171, v115
	s_waitcnt vmcnt(39)
	v_pk_add_f32 v[168:169], v[168:169], v[52:53]
	v_pk_add_f32 v[170:171], v[170:171], v[54:55]
	v_fma_f32 v172, s75, v168, -v52
	v_fma_f32 v173, s75, v169, -v53
	v_fma_f32 v174, s75, v170, -v54
	v_fma_f32 v175, s75, v171, -v55
	v_cvt_pk_bf16_f32 v176, v172, v173
	v_cvt_pk_bf16_f32 v177, v174, v175
	s_add_i32 s100, s73, 19
	s_lshl_b32 s98, s100, 12
	v_lshl_add_u64 v[178:179], v[2:3], 0, s[98:99]
	global_store_dwordx2 v[178:179], v[176:177], off sc1
	s_waitcnt vmcnt(39)
	v_sub_f32_e32 v168, v168, v116
	v_sub_f32_e32 v169, v169, v117
	v_sub_f32_e32 v170, v170, v118
	v_sub_f32_e32 v171, v171, v119
	s_waitcnt vmcnt(37)
	v_pk_add_f32 v[168:169], v[168:169], v[56:57]
	v_pk_add_f32 v[170:171], v[170:171], v[58:59]
	v_fma_f32 v172, s75, v168, -v56
	v_fma_f32 v173, s75, v169, -v57
	v_fma_f32 v174, s75, v170, -v58
	v_fma_f32 v175, s75, v171, -v59
	v_cvt_pk_bf16_f32 v176, v172, v173
	v_cvt_pk_bf16_f32 v177, v174, v175
	s_add_i32 s100, s73, 20
	s_lshl_b32 s98, s100, 12
	v_lshl_add_u64 v[178:179], v[2:3], 0, s[98:99]
	global_store_dwordx2 v[178:179], v[176:177], off sc1
	s_waitcnt vmcnt(37)
	v_sub_f32_e32 v168, v168, v120
	v_sub_f32_e32 v169, v169, v121
	v_sub_f32_e32 v170, v170, v122
	v_sub_f32_e32 v171, v171, v123
	s_waitcnt vmcnt(35)
	v_pk_add_f32 v[168:169], v[168:169], v[60:61]
	v_pk_add_f32 v[170:171], v[170:171], v[62:63]
	v_fma_f32 v172, s75, v168, -v60
	v_fma_f32 v173, s75, v169, -v61
	v_fma_f32 v174, s75, v170, -v62
	v_fma_f32 v175, s75, v171, -v63
	v_cvt_pk_bf16_f32 v176, v172, v173
	v_cvt_pk_bf16_f32 v177, v174, v175
	s_add_i32 s100, s73, 21
	s_lshl_b32 s98, s100, 12
	v_lshl_add_u64 v[178:179], v[2:3], 0, s[98:99]
	global_store_dwordx2 v[178:179], v[176:177], off sc1
	s_waitcnt vmcnt(35)
	v_sub_f32_e32 v168, v168, v124
	v_sub_f32_e32 v169, v169, v125
	v_sub_f32_e32 v170, v170, v126
	v_sub_f32_e32 v171, v171, v127
	s_waitcnt vmcnt(33)
	v_pk_add_f32 v[168:169], v[168:169], v[64:65]
	v_pk_add_f32 v[170:171], v[170:171], v[66:67]
	v_fma_f32 v172, s75, v168, -v64
	v_fma_f32 v173, s75, v169, -v65
	v_fma_f32 v174, s75, v170, -v66
	v_fma_f32 v175, s75, v171, -v67
	v_cvt_pk_bf16_f32 v176, v172, v173
	v_cvt_pk_bf16_f32 v177, v174, v175
	s_add_i32 s100, s73, 22
	s_lshl_b32 s98, s100, 12
	v_lshl_add_u64 v[178:179], v[2:3], 0, s[98:99]
	global_store_dwordx2 v[178:179], v[176:177], off sc1
	s_waitcnt vmcnt(33)
	v_sub_f32_e32 v168, v168, v128
	v_sub_f32_e32 v169, v169, v129
	v_sub_f32_e32 v170, v170, v130
	v_sub_f32_e32 v171, v171, v131
	s_waitcnt vmcnt(31)
	v_pk_add_f32 v[168:169], v[168:169], v[68:69]
	v_pk_add_f32 v[170:171], v[170:171], v[70:71]
	v_fma_f32 v172, s75, v168, -v68
	v_fma_f32 v173, s75, v169, -v69
	v_fma_f32 v174, s75, v170, -v70
	v_fma_f32 v175, s75, v171, -v71
	v_cvt_pk_bf16_f32 v176, v172, v173
	v_cvt_pk_bf16_f32 v177, v174, v175
	s_add_i32 s100, s73, 23
	s_lshl_b32 s98, s100, 12
	v_lshl_add_u64 v[178:179], v[2:3], 0, s[98:99]
	global_store_dwordx2 v[178:179], v[176:177], off sc1
	s_waitcnt vmcnt(31)
	v_sub_f32_e32 v168, v168, v132
	v_sub_f32_e32 v169, v169, v133
	v_sub_f32_e32 v170, v170, v134
	v_sub_f32_e32 v171, v171, v135
	s_waitcnt vmcnt(29)
	v_pk_add_f32 v[168:169], v[168:169], v[72:73]
	v_pk_add_f32 v[170:171], v[170:171], v[74:75]
	v_fma_f32 v172, s75, v168, -v72
	v_fma_f32 v173, s75, v169, -v73
	v_fma_f32 v174, s75, v170, -v74
	v_fma_f32 v175, s75, v171, -v75
	v_cvt_pk_bf16_f32 v176, v172, v173
	v_cvt_pk_bf16_f32 v177, v174, v175
	s_add_i32 s100, s73, 24
	s_lshl_b32 s98, s100, 12
	v_lshl_add_u64 v[178:179], v[2:3], 0, s[98:99]
	global_store_dwordx2 v[178:179], v[176:177], off sc1
	s_waitcnt vmcnt(29)
	v_sub_f32_e32 v168, v168, v136
	v_sub_f32_e32 v169, v169, v137
	v_sub_f32_e32 v170, v170, v138
	v_sub_f32_e32 v171, v171, v139
	s_waitcnt vmcnt(27)
	v_pk_add_f32 v[168:169], v[168:169], v[76:77]
	v_pk_add_f32 v[170:171], v[170:171], v[78:79]
	v_fma_f32 v172, s75, v168, -v76
	v_fma_f32 v173, s75, v169, -v77
	v_fma_f32 v174, s75, v170, -v78
	v_fma_f32 v175, s75, v171, -v79
	v_cvt_pk_bf16_f32 v176, v172, v173
	v_cvt_pk_bf16_f32 v177, v174, v175
	s_add_i32 s100, s73, 25
	s_lshl_b32 s98, s100, 12
	v_lshl_add_u64 v[178:179], v[2:3], 0, s[98:99]
	global_store_dwordx2 v[178:179], v[176:177], off sc1
	s_waitcnt vmcnt(27)
	v_sub_f32_e32 v168, v168, v140
	v_sub_f32_e32 v169, v169, v141
	v_sub_f32_e32 v170, v170, v142
	v_sub_f32_e32 v171, v171, v143
	s_waitcnt vmcnt(25)
	v_pk_add_f32 v[168:169], v[168:169], v[80:81]
	v_pk_add_f32 v[170:171], v[170:171], v[82:83]
	v_fma_f32 v172, s75, v168, -v80
	v_fma_f32 v173, s75, v169, -v81
	v_fma_f32 v174, s75, v170, -v82
	v_fma_f32 v175, s75, v171, -v83
	v_cvt_pk_bf16_f32 v176, v172, v173
	v_cvt_pk_bf16_f32 v177, v174, v175
	s_add_i32 s100, s73, 26
	s_lshl_b32 s98, s100, 12
	v_lshl_add_u64 v[178:179], v[2:3], 0, s[98:99]
	global_store_dwordx2 v[178:179], v[176:177], off sc1
	s_waitcnt vmcnt(25)
	v_sub_f32_e32 v168, v168, v144
	v_sub_f32_e32 v169, v169, v145
	v_sub_f32_e32 v170, v170, v146
	v_sub_f32_e32 v171, v171, v147
	s_waitcnt vmcnt(23)
	v_pk_add_f32 v[168:169], v[168:169], v[84:85]
	v_pk_add_f32 v[170:171], v[170:171], v[86:87]
	v_fma_f32 v172, s75, v168, -v84
	v_fma_f32 v173, s75, v169, -v85
	v_fma_f32 v174, s75, v170, -v86
	v_fma_f32 v175, s75, v171, -v87
	v_cvt_pk_bf16_f32 v176, v172, v173
	v_cvt_pk_bf16_f32 v177, v174, v175
	s_add_i32 s100, s73, 27
	s_lshl_b32 s98, s100, 12
	v_lshl_add_u64 v[178:179], v[2:3], 0, s[98:99]
	global_store_dwordx2 v[178:179], v[176:177], off sc1
	s_waitcnt vmcnt(23)
	v_sub_f32_e32 v168, v168, v148
	v_sub_f32_e32 v169, v169, v149
	v_sub_f32_e32 v170, v170, v150
	v_sub_f32_e32 v171, v171, v151
	s_waitcnt vmcnt(21)
	v_pk_add_f32 v[168:169], v[168:169], v[88:89]
	v_pk_add_f32 v[170:171], v[170:171], v[90:91]
	v_fma_f32 v172, s75, v168, -v88
	v_fma_f32 v173, s75, v169, -v89
	v_fma_f32 v174, s75, v170, -v90
	v_fma_f32 v175, s75, v171, -v91
	v_cvt_pk_bf16_f32 v176, v172, v173
	v_cvt_pk_bf16_f32 v177, v174, v175
	s_add_i32 s100, s73, 28
	s_lshl_b32 s98, s100, 12
	v_lshl_add_u64 v[178:179], v[2:3], 0, s[98:99]
	global_store_dwordx2 v[178:179], v[176:177], off sc1
	s_waitcnt vmcnt(21)
	v_sub_f32_e32 v168, v168, v152
	v_sub_f32_e32 v169, v169, v153
	v_sub_f32_e32 v170, v170, v154
	v_sub_f32_e32 v171, v171, v155
	s_waitcnt vmcnt(19)
	v_pk_add_f32 v[168:169], v[168:169], v[92:93]
	v_pk_add_f32 v[170:171], v[170:171], v[94:95]
	v_fma_f32 v172, s75, v168, -v92
	v_fma_f32 v173, s75, v169, -v93
	v_fma_f32 v174, s75, v170, -v94
	v_fma_f32 v175, s75, v171, -v95
	v_cvt_pk_bf16_f32 v176, v172, v173
	v_cvt_pk_bf16_f32 v177, v174, v175
	s_add_i32 s100, s73, 29
	s_lshl_b32 s98, s100, 12
	v_lshl_add_u64 v[178:179], v[2:3], 0, s[98:99]
	global_store_dwordx2 v[178:179], v[176:177], off sc1
	s_waitcnt vmcnt(19)
	v_sub_f32_e32 v168, v168, v156
	v_sub_f32_e32 v169, v169, v157
	v_sub_f32_e32 v170, v170, v158
	v_sub_f32_e32 v171, v171, v159
	s_waitcnt vmcnt(17)
	v_pk_add_f32 v[168:169], v[168:169], v[96:97]
	v_pk_add_f32 v[170:171], v[170:171], v[98:99]
	v_fma_f32 v172, s75, v168, -v96
	v_fma_f32 v173, s75, v169, -v97
	v_fma_f32 v174, s75, v170, -v98
	v_fma_f32 v175, s75, v171, -v99
	v_cvt_pk_bf16_f32 v176, v172, v173
	v_cvt_pk_bf16_f32 v177, v174, v175
	s_add_i32 s100, s73, 30
	s_lshl_b32 s98, s100, 12
	v_lshl_add_u64 v[178:179], v[2:3], 0, s[98:99]
	global_store_dwordx2 v[178:179], v[176:177], off sc1
	s_waitcnt vmcnt(17)
	v_sub_f32_e32 v168, v168, v160
	v_sub_f32_e32 v169, v169, v161
	v_sub_f32_e32 v170, v170, v162
	v_sub_f32_e32 v171, v171, v163
	s_waitcnt vmcnt(15)
	v_pk_add_f32 v[168:169], v[168:169], v[100:101]
	v_pk_add_f32 v[170:171], v[170:171], v[102:103]
	v_fma_f32 v172, s75, v168, -v100
	v_fma_f32 v173, s75, v169, -v101
	v_fma_f32 v174, s75, v170, -v102
	v_fma_f32 v175, s75, v171, -v103
	v_cvt_pk_bf16_f32 v176, v172, v173
	v_cvt_pk_bf16_f32 v177, v174, v175
	s_add_i32 s100, s73, 31
	s_lshl_b32 s98, s100, 12
	v_lshl_add_u64 v[178:179], v[2:3], 0, s[98:99]
	global_store_dwordx2 v[178:179], v[176:177], off sc1
	s_add_i32 s40, s40, s41
	s_cmpk_lt_i32 s40, 0x1000
	s_cbranch_scc1 .LBB0_236

.LBB0_416:
	s_waitcnt vmcnt(23)
	v_mov_b64_e32 v[50:51], v[34:35]
	s_waitcnt vmcnt(22)
	v_mov_b64_e32 v[56:57], v[36:37]
	v_lshlrev_b32_e32 v59, 16, v50
	v_lshlrev_b32_e32 v58, 16, v56
	v_and_b32_e32 v61, 0xffff0000, v50
	v_and_b32_e32 v60, 0xffff0000, v56
	v_lshlrev_b32_e32 v53, 16, v51
	v_lshlrev_b32_e32 v52, 16, v57
	v_and_b32_e32 v55, 0xffff0000, v51
	v_and_b32_e32 v54, 0xffff0000, v57
	v_pk_add_f32 v[50:51], v[58:59], v[60:61]
	v_pk_add_f32 v[56:57], v[52:53], v[54:55]
	s_waitcnt vmcnt(21)
	v_mov_b64_e32 v[62:63], v[38:39]
	v_pk_add_f32 v[50:51], v[50:51], v[56:57]
	s_waitcnt vmcnt(20)
	v_lshlrev_b32_e32 v44, 16, v27
	v_and_b32_e32 v45, 0xffff0000, v27
	v_add_f32_e32 v27, 0, v51
	v_add_f32_e32 v47, v50, v27
	v_lshlrev_b32_e32 v51, 16, v63
	v_lshlrev_b32_e32 v50, 16, v62
	v_and_b32_e32 v77, 0xffff0000, v63
	v_and_b32_e32 v76, 0xffff0000, v62
	v_pk_add_f32 v[56:57], v[50:51], v[76:77]
	v_lshlrev_b32_e32 v42, 16, v26
	v_and_b32_e32 v43, 0xffff0000, v26
	v_pk_add_f32 v[56:57], v[56:57], v[56:57] op_sel_hi:[0,1]
	s_waitcnt vmcnt(18)
	v_mov_b64_e32 v[64:65], v[40:41]
	v_lshlrev_b32_e32 v40, 16, v32
	v_and_b32_e32 v48, 0xffff0000, v32
	v_lshlrev_b32_e32 v38, 16, v33
	v_and_b32_e32 v46, 0xffff0000, v33
	v_add_f32_e32 v41, v42, v43
	v_add_f32_e32 v49, v44, v45
	v_mov_b32_e32 v39, v57
	v_pk_add_f32 v[62:63], v[40:41], v[48:49]
	v_pk_add_f32 v[56:57], v[38:39], v[46:47]
	v_and_b32_e32 v79, 0xffff0000, v65
	v_pk_add_f32 v[56:57], v[62:63], v[56:57]
	v_and_b32_e32 v78, 0xffff0000, v64
	v_pk_add_f32 v[62:63], v[56:57], v[56:57] op_sel_hi:[0,1]
	v_lshlrev_b32_e32 v57, 16, v65
	v_lshlrev_b32_e32 v56, 16, v64
	v_pk_add_f32 v[64:65], v[56:57], v[78:79]
	s_waitcnt vmcnt(17)
	v_lshlrev_b32_e32 v32, 16, v28
	v_and_b32_e32 v33, 0xffff0000, v28
	v_lshlrev_b32_e32 v36, 16, v29
	v_and_b32_e32 v37, 0xffff0000, v29
	v_pk_add_f32 v[64:65], v[64:65], v[64:65] op_sel_hi:[0,1]
	s_waitcnt vmcnt(16)
	v_lshlrev_b32_e32 v28, 16, v30
	v_and_b32_e32 v34, 0xffff0000, v30
	v_lshlrev_b32_e32 v26, 16, v31
	v_and_b32_e32 v30, 0xffff0000, v31
	v_add_f32_e32 v29, v32, v33
	v_add_f32_e32 v35, v36, v37
	v_mov_b32_e32 v27, v65
	v_mov_b32_e32 v31, v63
	v_pk_add_f32 v[80:81], v[28:29], v[34:35]
	v_pk_add_f32 v[62:63], v[26:27], v[30:31]
	s_nop 0
	v_pk_add_f32 v[62:63], v[80:81], v[62:63]
	s_nop 0
	v_add_f32_e32 v27, v62, v63
	ds_bpermute_b32 v29, v66, v27
	s_waitcnt lgkmcnt(0)
	v_add_f32_e32 v27, v27, v29
	ds_bpermute_b32 v29, v67, v27
	s_waitcnt lgkmcnt(0)
	v_add_f32_e32 v27, v27, v29
	ds_bpermute_b32 v29, v68, v27
	s_waitcnt lgkmcnt(0)
	v_add_f32_e32 v27, v27, v29
	ds_bpermute_b32 v29, v69, v27
	s_waitcnt lgkmcnt(0)
	v_add_f32_e32 v27, v27, v29
	ds_bpermute_b32 v29, v70, v27
	s_waitcnt lgkmcnt(0)
	v_add_f32_e32 v27, v27, v29
	ds_bpermute_b32 v29, v71, v27
	s_waitcnt lgkmcnt(0)
	v_add_f32_e32 v27, v27, v29
	v_fmac_f32_e32 v61, 0xba000000, v27
	v_fmac_f32_e32 v60, 0xba000000, v27
	v_fmac_f32_e32 v55, 0xba000000, v27
	v_fmac_f32_e32 v59, 0xba000000, v27
	v_fmac_f32_e32 v54, 0xba000000, v27
	v_fmac_f32_e32 v58, 0xba000000, v27
	v_mov_b32_e32 v64, v61
	v_mov_b32_e32 v65, v60
	v_fmac_f32_e32 v53, 0xba000000, v27
	v_fmac_f32_e32 v52, 0xba000000, v27
	v_mov_b32_e32 v62, v59
	v_mov_b32_e32 v63, v58
	v_pk_mul_f32 v[64:65], v[64:65], v[64:65]
	v_mov_b32_e32 v80, v55
	v_mov_b32_e32 v81, v54
	v_pk_fma_f32 v[62:63], v[62:63], v[62:63], v[64:65]
	v_mov_b32_e32 v64, v53
	v_mov_b32_e32 v65, v52
	v_pk_mul_f32 v[80:81], v[80:81], v[80:81]
	v_fmac_f32_e32 v76, 0xba000000, v27
	v_pk_fma_f32 v[64:65], v[64:65], v[64:65], v[80:81]
	v_fmac_f32_e32 v77, 0xba000000, v27
	v_pk_add_f32 v[62:63], v[62:63], v[64:65]
	v_fmac_f32_e32 v51, 0xba000000, v27
	v_pk_add_f32 v[64:65], v[62:63], v[62:63] op_sel_hi:[0,1]
	v_fmac_f32_e32 v50, 0xba000000, v27
	v_mov_b32_e32 v62, v51
	v_mov_b32_e32 v63, v77
	v_mov_b32_e32 v51, v76
	v_pk_mul_f32 v[80:81], v[62:63], v[62:63]
	v_pk_mul_f32 v[76:77], v[50:51], v[50:51]
	v_fmac_f32_e32 v42, 0xba000000, v27
	v_pk_mov_b32 v[82:83], v[76:77], v[80:81] op_sel:[1,0]
	v_mov_b32_e32 v77, v81
	v_fmac_f32_e32 v43, 0xba000000, v27
	v_fmac_f32_e32 v44, 0xba000000, v27
	v_mul_f32_e32 v64, v42, v42
	v_pk_add_f32 v[76:77], v[82:83], v[76:77]
	v_fmac_f32_e32 v45, 0xba000000, v27
	v_pk_fma_f32 v[80:81], v[42:43], v[42:43], v[64:65] op_sel_hi:[1,1,0]
	v_mul_f32_e32 v64, v44, v44
	v_pk_add_f32 v[76:77], v[76:77], v[76:77] op_sel_hi:[0,1]
	v_pk_fma_f32 v[82:83], v[44:45], v[44:45], v[64:65] op_sel_hi:[1,1,0]
	v_fmac_f32_e32 v46, 0xba000000, v27
	v_fmac_f32_e32 v38, 0xba000000, v27
	v_fmac_f32_e32 v48, 0xba000000, v27
	v_fmac_f32_e32 v40, 0xba000000, v27
	v_mul_f32_e32 v80, v40, v40
	v_mul_f32_e32 v82, v48, v48
	v_mul_f32_e32 v76, v38, v38
	v_mul_f32_e32 v64, v46, v46
	v_pk_add_f32 v[80:81], v[80:81], v[82:83]
	v_pk_add_f32 v[64:65], v[76:77], v[64:65]
	v_fmac_f32_e32 v78, 0xba000000, v27
	v_pk_add_f32 v[64:65], v[80:81], v[64:65]
	v_fmac_f32_e32 v79, 0xba000000, v27
	v_fmac_f32_e32 v57, 0xba000000, v27
	v_pk_add_f32 v[76:77], v[64:65], v[64:65] op_sel_hi:[0,1]
	v_fmac_f32_e32 v56, 0xba000000, v27
	v_mov_b32_e32 v64, v57
	v_mov_b32_e32 v65, v79
	v_mov_b32_e32 v57, v78
	v_pk_mul_f32 v[80:81], v[64:65], v[64:65]
	v_pk_mul_f32 v[78:79], v[56:57], v[56:57]
	v_fmac_f32_e32 v32, 0xba000000, v27
	v_pk_mov_b32 v[82:83], v[78:79], v[80:81] op_sel:[1,0]
	v_mov_b32_e32 v79, v81
	v_fmac_f32_e32 v33, 0xba000000, v27
	v_fmac_f32_e32 v36, 0xba000000, v27
	v_mul_f32_e32 v76, v32, v32
	v_pk_add_f32 v[78:79], v[82:83], v[78:79]
	v_fmac_f32_e32 v37, 0xba000000, v27
	v_pk_fma_f32 v[80:81], v[32:33], v[32:33], v[76:77] op_sel_hi:[1,1,0]
	v_mul_f32_e32 v76, v36, v36
	v_pk_add_f32 v[78:79], v[78:79], v[78:79] op_sel_hi:[0,1]
	v_pk_fma_f32 v[82:83], v[36:37], v[36:37], v[76:77] op_sel_hi:[1,1,0]
	v_fmac_f32_e32 v30, 0xba000000, v27
	v_fmac_f32_e32 v26, 0xba000000, v27
	v_fmac_f32_e32 v34, 0xba000000, v27
	v_fmac_f32_e32 v28, 0xba000000, v27
	v_mul_f32_e32 v80, v28, v28
	v_mul_f32_e32 v82, v34, v34
	v_mul_f32_e32 v78, v26, v26
	v_mul_f32_e32 v76, v30, v30
	v_pk_add_f32 v[80:81], v[80:81], v[82:83]
	v_pk_add_f32 v[76:77], v[78:79], v[76:77]
	v_mov_b32_e32 v140, v58
	v_pk_add_f32 v[76:77], v[80:81], v[76:77]
	v_mov_b32_e32 v141, v60
	v_add_f32_e32 v27, v76, v77
	global_load_dwordx4 v[76:79], v[2:3], off
	global_load_dwordx4 v[80:83], v[4:5], off
	global_load_dwordx4 v[84:87], v[2:3], off offset:1024
	global_load_dwordx4 v[88:91], v[4:5], off offset:1024
	global_load_dwordx4 v[92:95], v[2:3], off offset:2048
	global_load_dwordx4 v[96:99], v[4:5], off offset:2048
	global_load_dwordx4 v[100:103], v[2:3], off offset:3072
	global_load_dwordx4 v[104:107], v[4:5], off offset:3072
	global_load_dwordx4 v[108:111], v[6:7], off
	global_load_dwordx4 v[112:115], v[8:9], off
	global_load_dwordx4 v[116:119], v[10:11], off
	global_load_dwordx4 v[120:123], v[12:13], off
	global_load_dwordx4 v[124:127], v[14:15], off
	global_load_dwordx4 v[128:131], v[16:17], off
	global_load_dwordx4 v[132:135], v[18:19], off
	global_load_dwordx4 v[136:139], v[20:21], off
	ds_bpermute_b32 v29, v66, v27
	v_mov_b32_e32 v60, v59
	v_mov_b32_e32 v58, v52
	v_mov_b32_e32 v59, v54
	v_mov_b32_e32 v54, v53
	s_waitcnt lgkmcnt(0)
	v_add_f32_e32 v27, v27, v29
	ds_bpermute_b32 v29, v67, v27
	s_waitcnt lgkmcnt(0)
	v_add_f32_e32 v27, v27, v29
	ds_bpermute_b32 v29, v68, v27
	s_waitcnt lgkmcnt(0)
	v_add_f32_e32 v27, v27, v29
	ds_bpermute_b32 v29, v69, v27
	s_waitcnt lgkmcnt(0)
	v_add_f32_e32 v27, v27, v29
	ds_bpermute_b32 v29, v70, v27
	s_waitcnt lgkmcnt(0)
	v_add_f32_e32 v27, v27, v29
	ds_bpermute_b32 v29, v71, v27
	s_waitcnt lgkmcnt(0)
	v_add_f32_e32 v27, v27, v29
	v_fmamk_f32 v27, v27, 0x3a000000, v72
	v_mul_f32_e32 v29, 0x4f800000, v27
	v_cmp_gt_f32_e32 vcc, s7, v27
	s_nop 1
	v_cndmask_b32_e32 v27, v27, v29, vcc
	v_sqrt_f32_e32 v29, v27
	s_nop 0
	v_add_u32_e32 v31, -1, v29
	v_fma_f32 v35, -v31, v29, v27
	v_cmp_ge_f32_e64 s[2:3], 0, v35
	v_add_u32_e32 v35, 1, v29
	s_nop 0
	v_cndmask_b32_e64 v31, v29, v31, s[2:3]
	v_fma_f32 v29, -v35, v29, v27
	v_cmp_lt_f32_e64 s[2:3], 0, v29
	s_nop 1
	v_cndmask_b32_e64 v29, v31, v35, s[2:3]
	v_mul_f32_e32 v31, 0x37800000, v29
	v_cndmask_b32_e32 v29, v29, v31, vcc
	v_cmp_class_f32_e32 vcc, v27, v73
	s_nop 1
	v_cndmask_b32_e32 v27, v29, v27, vcc
	v_div_scale_f32 v29, s[2:3], v27, v27, 1.0
	v_rcp_f32_e32 v31, v29
	s_mov_b32 s2, s6
	s_add_i32 s6, s6, s8
	s_cmpk_gt_i32 s6, 0x3fff
	v_fma_f32 v35, -v29, v31, 1.0
	v_fmac_f32_e32 v31, v35, v31
	v_div_scale_f32 v35, vcc, 1.0, v27, 1.0
	v_mul_f32_e32 v39, v35, v31
	v_fma_f32 v41, -v29, v39, v35
	v_fmac_f32_e32 v39, v41, v31
	v_fma_f32 v29, -v29, v39, v35
	v_div_fmas_f32 v29, v29, v31, v39
	v_div_fixup_f32 v52, v29, v27, 1.0
	v_pk_mul_f32 v[60:61], v[60:61], v[52:53] op_sel_hi:[1,0]
	v_pk_mul_f32 v[54:55], v[54:55], v[52:53] op_sel_hi:[1,0]
	v_mov_b32_e32 v41, v48
	v_mov_b32_e32 v39, v46
	v_mov_b32_e32 v27, v30
	s_waitcnt vmcnt(14)
	v_pk_fma_f32 v[54:55], v[78:79], v[54:55], v[82:83]
	v_pk_fma_f32 v[60:61], v[76:77], v[60:61], v[80:81]
	v_pk_mul_f32 v[76:77], v[140:141], v[52:53] op_sel_hi:[1,0]
	v_pk_mul_f32 v[58:59], v[58:59], v[52:53] op_sel_hi:[1,0]
	v_pk_mul_f32 v[40:41], v[40:41], v[52:53] op_sel_hi:[1,0]
	v_pk_mul_f32 v[38:39], v[38:39], v[52:53] op_sel_hi:[1,0]
	v_mov_b32_e32 v29, v34
	v_pk_mul_f32 v[26:27], v[26:27], v[52:53] op_sel_hi:[1,0]
	s_waitcnt vmcnt(12)
	v_pk_fma_f32 v[58:59], v[86:87], v[58:59], v[90:91]
	v_pk_fma_f32 v[76:77], v[84:85], v[76:77], v[88:89]
	v_pk_mul_f32 v[50:51], v[50:51], v[52:53] op_sel_hi:[1,0]
	v_pk_mul_f32 v[62:63], v[62:63], v[52:53] op_sel_hi:[1,0]
	v_pk_mul_f32 v[42:43], v[42:43], v[52:53] op_sel_hi:[1,0]
	v_pk_mul_f32 v[44:45], v[44:45], v[52:53] op_sel_hi:[1,0]
	s_waitcnt vmcnt(6)
	v_pk_fma_f32 v[46:47], v[110:111], v[38:39], v[114:115]
	v_pk_fma_f32 v[48:49], v[108:109], v[40:41], v[112:113]
	v_pk_mul_f32 v[38:39], v[56:57], v[52:53] op_sel_hi:[1,0]
	v_pk_mul_f32 v[40:41], v[64:65], v[52:53] op_sel_hi:[1,0]
	v_pk_mul_f32 v[32:33], v[32:33], v[52:53] op_sel_hi:[1,0]
	v_pk_mul_f32 v[36:37], v[36:37], v[52:53] op_sel_hi:[1,0]
	v_pk_mul_f32 v[28:29], v[28:29], v[52:53] op_sel_hi:[1,0]
	s_waitcnt vmcnt(0)
	v_pk_fma_f32 v[52:53], v[134:135], v[26:27], v[138:139]
	v_max_f32_e64 v26, |v60|, |v61|
	v_max_f32_e64 v27, |v54|, |v55|
	v_pk_fma_f32 v[62:63], v[94:95], v[62:63], v[98:99]
	v_pk_fma_f32 v[50:51], v[92:93], v[50:51], v[96:97]
	v_pk_fma_f32 v[84:85], v[132:133], v[28:29], v[136:137]
	v_max3_f32 v26, v26, 0, v27
	v_max_f32_e64 v27, |v76|, |v77|
	v_max_f32_e64 v28, |v58|, |v59|
	v_pk_fma_f32 v[44:45], v[102:103], v[44:45], v[106:107]
	v_pk_fma_f32 v[78:79], v[100:101], v[42:43], v[104:105]
	v_max3_f32 v26, v26, v27, v28
	v_max_f32_e64 v27, |v50|, |v51|
	v_max_f32_e64 v28, |v62|, |v63|
	v_max3_f32 v26, v26, v27, v28
	v_max_f32_e64 v27, |v78|, |v79|
	v_max_f32_e64 v28, |v44|, |v45|
	v_pk_fma_f32 v[56:57], v[118:119], v[40:41], v[122:123]
	v_pk_fma_f32 v[64:65], v[116:117], v[38:39], v[120:121]
	v_max3_f32 v26, v26, v27, v28
	v_max_f32_e64 v27, |v48|, |v49|
	v_max_f32_e64 v28, |v46|, |v47|
	v_pk_fma_f32 v[80:81], v[126:127], v[36:37], v[130:131]
	v_pk_fma_f32 v[82:83], v[124:125], v[32:33], v[128:129]
	v_max3_f32 v26, v26, v27, v28
	v_max_f32_e64 v27, |v64|, |v65|
	v_max_f32_e64 v28, |v56|, |v57|
	v_max3_f32 v26, v26, v27, v28
	v_max_f32_e64 v27, |v82|, |v83|
	v_max_f32_e64 v28, |v80|, |v81|
	v_max3_f32 v26, v26, v27, v28
	v_max_f32_e64 v27, |v84|, |v85|
	v_max_f32_e64 v28, |v52|, |v53|
	v_max3_f32 v26, v26, v27, v28
	ds_bpermute_b32 v27, v66, v26
	s_cselect_b64 s[16:17], -1, 0
	s_cmpk_lt_i32 s6, 0x4000
	s_cselect_b32 s2, s6, s2
	s_ashr_i32 s3, s2, 31
	s_waitcnt lgkmcnt(0)
	v_max_f32_e32 v27, v27, v27
	v_max_f32_e32 v26, v26, v27
	ds_bpermute_b32 v27, v67, v26
	s_lshl_b64 s[2:3], s[2:3], 12
	v_lshl_add_u64 v[86:87], v[0:1], 0, s[2:3]
	s_waitcnt lgkmcnt(0)
	v_max_f32_e32 v27, v27, v27
	v_max_f32_e32 v26, v26, v27
	ds_bpermute_b32 v27, v68, v26
	s_waitcnt lgkmcnt(0)
	v_max_f32_e32 v27, v27, v27
	v_max_f32_e32 v26, v26, v27
	ds_bpermute_b32 v27, v69, v26
	s_waitcnt lgkmcnt(0)
	v_max_f32_e32 v27, v27, v27
	v_max_f32_e32 v26, v26, v27
	ds_bpermute_b32 v27, v70, v26
	s_waitcnt lgkmcnt(0)
	v_max_f32_e32 v27, v27, v27
	v_max_f32_e32 v28, v26, v27
	ds_bpermute_b32 v29, v71, v28
	global_load_dwordx2 v[34:35], v[86:87], off
	global_load_dwordx2 v[36:37], v[86:87], off offset:512
	global_load_dwordx2 v[38:39], v[86:87], off offset:1024
	global_load_dwordx2 v[26:27], v[86:87], off offset:1536
	s_waitcnt lgkmcnt(0)
	v_max_f32_e32 v29, v29, v29
	v_max_f32_e32 v42, v28, v29
	global_load_dwordx2 v[32:33], v[86:87], off offset:2048
	global_load_dwordx2 v[40:41], v[86:87], off offset:2560
	global_load_dwordx2 v[28:29], v[86:87], off offset:3072
	global_load_dwordx2 v[30:31], v[86:87], off offset:3584
	v_div_scale_f32 v43, s[2:3], v42, v42, s9
	v_rcp_f32_e32 v75, v43
	v_cvt_pk_bf16_f32 v90, v60, v61
	v_cvt_pk_bf16_f32 v91, v54, v55
	s_nop 0
	v_fma_f32 v86, -v43, v75, 1.0
	v_fmac_f32_e32 v75, v86, v75
	v_div_scale_f32 v86, vcc, s9, v42, s9
	v_mul_f32_e32 v87, v86, v75
	v_fma_f32 v88, -v43, v87, v86
	v_fmac_f32_e32 v87, v88, v75
	v_fma_f32 v43, -v43, v87, v86
	v_div_fmas_f32 v43, v43, v75, v87
	v_div_fixup_f32 v43, v43, v42, s9
	v_cmp_lt_f32_e32 vcc, 0, v42
	v_lshl_add_u64 v[86:87], s[66:67], 0, v[22:23]
	v_add_co_u32_e64 v86, s[2:3], s20, v86
	v_cndmask_b32_e32 v43, 0, v43, vcc
	v_fmaak_f32 v60, v60, v43, 0x4b400000
	v_fmaak_f32 v61, v61, v43, 0x4b400000
	v_fmaak_f32 v54, v54, v43, 0x4b400000
	v_fmaak_f32 v55, v55, v43, 0x4b400000
	v_lshl_add_u64 v[88:89], s[66:67], 0, v[24:25]
	v_addc_co_u32_e64 v87, s[2:3], 0, v87, s[2:3]
	v_perm_b32 v60, v61, v60, s21
	v_perm_b32 v54, v55, v54, s22
	v_or_b32_e32 v60, v54, v60
	v_add_co_u32_e64 v54, s[2:3], s23, v88
	global_store_dwordx2 v[86:87], v[90:91], off sc1
	s_nop 0
	v_addc_co_u32_e64 v55, s[2:3], 0, v89, s[2:3]
	global_store_dword v[54:55], v60, off sc1
	v_cvt_pk_bf16_f32 v60, v76, v77
	v_cvt_pk_bf16_f32 v61, v58, v59
	global_store_dwordx2 v[86:87], v[60:61], off offset:512 sc1
	v_fmaak_f32 v60, v76, v43, 0x4b400000
	v_fmaak_f32 v61, v77, v43, 0x4b400000
	v_fmaak_f32 v58, v58, v43, 0x4b400000
	v_fmaak_f32 v59, v59, v43, 0x4b400000
	v_perm_b32 v60, v61, v60, s21
	v_perm_b32 v58, v59, v58, s22
	v_or_b32_e32 v58, v58, v60
	global_store_dword v[54:55], v58, off offset:256 sc1
	v_cvt_pk_bf16_f32 v58, v50, v51
	v_cvt_pk_bf16_f32 v59, v62, v63
	global_store_dwordx2 v[86:87], v[58:59], off offset:1024 sc1
	v_fmaak_f32 v50, v50, v43, 0x4b400000
	v_fmaak_f32 v51, v51, v43, 0x4b400000
	v_fmaak_f32 v58, v62, v43, 0x4b400000
	v_fmaak_f32 v59, v63, v43, 0x4b400000
	v_perm_b32 v50, v51, v50, s21
	v_perm_b32 v51, v59, v58, s22
	v_or_b32_e32 v50, v51, v50
	global_store_dword v[54:55], v50, off offset:512 sc1
	v_cvt_pk_bf16_f32 v50, v78, v79
	v_cvt_pk_bf16_f32 v51, v44, v45
	global_store_dwordx2 v[86:87], v[50:51], off offset:1536 sc1
	v_fmaak_f32 v50, v78, v43, 0x4b400000
	v_fmaak_f32 v51, v79, v43, 0x4b400000
	v_fmaak_f32 v44, v44, v43, 0x4b400000
	v_fmaak_f32 v45, v45, v43, 0x4b400000
	v_perm_b32 v50, v51, v50, s21
	v_perm_b32 v44, v45, v44, s22
	v_or_b32_e32 v44, v44, v50
	global_store_dword v[54:55], v44, off offset:768 sc1
	v_cvt_pk_bf16_f32 v44, v48, v49
	v_cvt_pk_bf16_f32 v45, v46, v47
	global_store_dwordx2 v[86:87], v[44:45], off offset:2048 sc1
	v_fmaak_f32 v44, v48, v43, 0x4b400000
	v_fmaak_f32 v45, v49, v43, 0x4b400000
	v_fmaak_f32 v46, v46, v43, 0x4b400000
	v_fmaak_f32 v47, v47, v43, 0x4b400000
	v_perm_b32 v44, v45, v44, s21
	v_perm_b32 v45, v47, v46, s22
	v_or_b32_e32 v44, v45, v44
	global_store_dword v[54:55], v44, off offset:1024 sc1
	v_cvt_pk_bf16_f32 v44, v64, v65
	v_cvt_pk_bf16_f32 v45, v56, v57
	global_store_dwordx2 v[86:87], v[44:45], off offset:2560 sc1
	v_fmaak_f32 v44, v64, v43, 0x4b400000
	v_fmaak_f32 v45, v65, v43, 0x4b400000
	v_fmaak_f32 v46, v56, v43, 0x4b400000
	v_fmaak_f32 v47, v57, v43, 0x4b400000
	v_perm_b32 v44, v45, v44, s21
	v_perm_b32 v45, v47, v46, s22
	v_or_b32_e32 v44, v45, v44
	global_store_dword v[54:55], v44, off offset:1280 sc1
	v_cvt_pk_bf16_f32 v44, v82, v83
	v_cvt_pk_bf16_f32 v45, v80, v81
	global_store_dwordx2 v[86:87], v[44:45], off offset:3072 sc1
	v_fmaak_f32 v44, v82, v43, 0x4b400000
	v_fmaak_f32 v45, v83, v43, 0x4b400000
	v_fmaak_f32 v46, v80, v43, 0x4b400000
	v_fmaak_f32 v47, v81, v43, 0x4b400000
	v_perm_b32 v44, v45, v44, s21
	v_perm_b32 v45, v47, v46, s22
	v_or_b32_e32 v44, v45, v44
	global_store_dword v[54:55], v44, off offset:1536 sc1
	v_cvt_pk_bf16_f32 v44, v84, v85
	v_cvt_pk_bf16_f32 v45, v52, v53
	global_store_dwordx2 v[86:87], v[44:45], off offset:3584 sc1
	v_fmaak_f32 v44, v84, v43, 0x4b400000
	v_fmaak_f32 v45, v85, v43, 0x4b400000
	v_fmaak_f32 v46, v52, v43, 0x4b400000
	v_fmaak_f32 v43, v53, v43, 0x4b400000
	v_perm_b32 v44, v45, v44, s21
	v_perm_b32 v43, v43, v46, s22
	v_or_b32_e32 v43, v43, v44
	global_store_dword v[54:55], v43, off offset:1792 sc1
	s_and_saveexec_b64 s[2:3], s[0:1]
	s_cbranch_execz .LBB0_415
	s_add_u32 s24, s66, s18
	v_mul_f32_e32 v42, 0x3c010204, v42
	s_addc_u32 s25, s67, s19
	v_cndmask_b32_e32 v42, 1.0, v42, vcc
	global_store_dword v74, v42, s[24:25]
	s_branch .LBB0_415

.LBB0_1694:
	s_waitcnt vmcnt(23)
	v_mov_b64_e32 v[52:53], v[36:37]
	s_waitcnt vmcnt(22)
	v_mov_b64_e32 v[62:63], v[38:39]
	s_waitcnt lgkmcnt(0)
	v_lshlrev_b32_e32 v59, 16, v52
	v_lshlrev_b32_e32 v58, 16, v62
	v_and_b32_e32 v61, 0xffff0000, v52
	v_and_b32_e32 v60, 0xffff0000, v62
	v_lshlrev_b32_e32 v55, 16, v53
	v_lshlrev_b32_e32 v54, 16, v63
	v_and_b32_e32 v57, 0xffff0000, v53
	v_and_b32_e32 v56, 0xffff0000, v63
	v_pk_add_f32 v[52:53], v[58:59], v[60:61]
	v_pk_add_f32 v[62:63], v[54:55], v[56:57]
	s_waitcnt vmcnt(21)
	v_mov_b64_e32 v[64:65], v[40:41]
	v_pk_add_f32 v[52:53], v[52:53], v[62:63]
	s_waitcnt vmcnt(20)
	v_lshlrev_b32_e32 v46, 16, v29
	v_and_b32_e32 v47, 0xffff0000, v29
	v_add_f32_e32 v29, 0, v53
	v_add_f32_e32 v49, v52, v29
	v_lshlrev_b32_e32 v53, 16, v65
	v_lshlrev_b32_e32 v52, 16, v64
	v_and_b32_e32 v65, 0xffff0000, v65
	v_and_b32_e32 v64, 0xffff0000, v64
	v_pk_add_f32 v[62:63], v[52:53], v[64:65]
	v_lshlrev_b32_e32 v44, 16, v28
	v_and_b32_e32 v45, 0xffff0000, v28
	v_pk_add_f32 v[62:63], v[62:63], v[62:63] op_sel_hi:[0,1]
	s_waitcnt vmcnt(18)
	v_mov_b64_e32 v[66:67], v[42:43]
	v_lshlrev_b32_e32 v42, 16, v34
	v_and_b32_e32 v50, 0xffff0000, v34
	v_lshlrev_b32_e32 v40, 16, v35
	v_and_b32_e32 v48, 0xffff0000, v35
	v_add_f32_e32 v43, v44, v45
	v_add_f32_e32 v51, v46, v47
	v_mov_b32_e32 v41, v63
	v_pk_add_f32 v[68:69], v[42:43], v[50:51]
	v_pk_add_f32 v[62:63], v[40:41], v[48:49]
	v_lshlrev_b32_e32 v73, 16, v67
	v_lshlrev_b32_e32 v72, 16, v66
	v_and_b32_e32 v67, 0xffff0000, v67
	v_and_b32_e32 v66, 0xffff0000, v66
	v_pk_add_f32 v[62:63], v[68:69], v[62:63]
	v_pk_add_f32 v[68:69], v[72:73], v[66:67]
	s_waitcnt vmcnt(17)
	v_lshlrev_b32_e32 v34, 16, v32
	v_and_b32_e32 v35, 0xffff0000, v32
	v_lshlrev_b32_e32 v38, 16, v33
	v_and_b32_e32 v39, 0xffff0000, v33
	v_pk_add_f32 v[62:63], v[62:63], v[62:63] op_sel_hi:[0,1]
	v_pk_add_f32 v[68:69], v[68:69], v[68:69] op_sel_hi:[0,1]
	s_waitcnt vmcnt(16)
	v_lshlrev_b32_e32 v32, 16, v30
	v_and_b32_e32 v36, 0xffff0000, v30
	v_lshlrev_b32_e32 v28, 16, v31
	v_and_b32_e32 v30, 0xffff0000, v31
	v_add_f32_e32 v33, v34, v35
	v_add_f32_e32 v37, v38, v39
	v_mov_b32_e32 v29, v69
	v_mov_b32_e32 v31, v63
	v_pk_add_f32 v[70:71], v[32:33], v[36:37]
	v_pk_add_f32 v[62:63], v[28:29], v[30:31]
	s_nop 0
	v_pk_add_f32 v[62:63], v[70:71], v[62:63]
	s_nop 0
	v_add_f32_e32 v29, v62, v63
	ds_bpermute_b32 v31, v82, v29
	s_waitcnt lgkmcnt(0)
	v_add_f32_e32 v29, v29, v31
	ds_bpermute_b32 v31, v83, v29
	s_waitcnt lgkmcnt(0)
	v_add_f32_e32 v29, v29, v31
	ds_bpermute_b32 v31, v84, v29
	s_waitcnt lgkmcnt(0)
	v_add_f32_e32 v29, v29, v31
	ds_bpermute_b32 v31, v85, v29
	s_waitcnt lgkmcnt(0)
	v_add_f32_e32 v29, v29, v31
	ds_bpermute_b32 v31, v86, v29
	s_waitcnt lgkmcnt(0)
	v_add_f32_e32 v29, v29, v31
	ds_bpermute_b32 v31, v87, v29
	s_waitcnt lgkmcnt(0)
	v_add_f32_e32 v29, v29, v31
	v_fmac_f32_e32 v61, 0xba000000, v29
	v_fmac_f32_e32 v60, 0xba000000, v29
	v_fmac_f32_e32 v57, 0xba000000, v29
	v_fmac_f32_e32 v59, 0xba000000, v29
	v_fmac_f32_e32 v56, 0xba000000, v29
	v_fmac_f32_e32 v58, 0xba000000, v29
	v_mov_b32_e32 v68, v61
	v_mov_b32_e32 v69, v60
	v_fmac_f32_e32 v55, 0xba000000, v29
	v_fmac_f32_e32 v54, 0xba000000, v29
	v_mov_b32_e32 v62, v59
	v_mov_b32_e32 v63, v58
	v_pk_mul_f32 v[68:69], v[68:69], v[68:69]
	v_mov_b32_e32 v70, v57
	v_mov_b32_e32 v71, v56
	v_pk_fma_f32 v[62:63], v[62:63], v[62:63], v[68:69]
	v_mov_b32_e32 v68, v55
	v_mov_b32_e32 v69, v54
	v_pk_mul_f32 v[70:71], v[70:71], v[70:71]
	v_fmac_f32_e32 v64, 0xba000000, v29
	v_pk_fma_f32 v[68:69], v[68:69], v[68:69], v[70:71]
	v_fmac_f32_e32 v65, 0xba000000, v29
	v_pk_add_f32 v[62:63], v[62:63], v[68:69]
	v_fmac_f32_e32 v53, 0xba000000, v29
	v_pk_add_f32 v[68:69], v[62:63], v[62:63] op_sel_hi:[0,1]
	v_fmac_f32_e32 v52, 0xba000000, v29
	v_mov_b32_e32 v62, v53
	v_mov_b32_e32 v63, v65
	v_mov_b32_e32 v53, v64
	v_pk_mul_f32 v[70:71], v[62:63], v[62:63]
	v_pk_mul_f32 v[64:65], v[52:53], v[52:53]
	v_fmac_f32_e32 v44, 0xba000000, v29
	v_pk_mov_b32 v[74:75], v[64:65], v[70:71] op_sel:[1,0]
	v_mov_b32_e32 v65, v71
	v_pk_add_f32 v[64:65], v[74:75], v[64:65]
	v_fmac_f32_e32 v45, 0xba000000, v29
	v_pk_add_f32 v[64:65], v[64:65], v[64:65] op_sel_hi:[0,1]
	v_fmac_f32_e32 v46, 0xba000000, v29
	v_mul_f32_e32 v64, v44, v44
	v_fmac_f32_e32 v47, 0xba000000, v29
	v_pk_fma_f32 v[70:71], v[44:45], v[44:45], v[64:65] op_sel_hi:[1,1,0]
	v_mul_f32_e32 v64, v46, v46
	v_pk_fma_f32 v[74:75], v[46:47], v[46:47], v[64:65] op_sel_hi:[1,1,0]
	v_fmac_f32_e32 v48, 0xba000000, v29
	v_fmac_f32_e32 v40, 0xba000000, v29
	v_fmac_f32_e32 v50, 0xba000000, v29
	v_fmac_f32_e32 v42, 0xba000000, v29
	v_mul_f32_e32 v70, v42, v42
	v_mul_f32_e32 v74, v50, v50
	v_mul_f32_e32 v64, v40, v40
	v_mul_f32_e32 v68, v48, v48
	v_pk_add_f32 v[70:71], v[70:71], v[74:75]
	v_pk_add_f32 v[64:65], v[64:65], v[68:69]
	v_fmac_f32_e32 v66, 0xba000000, v29
	v_fmac_f32_e32 v67, 0xba000000, v29
	v_fmac_f32_e32 v73, 0xba000000, v29
	v_pk_add_f32 v[64:65], v[70:71], v[64:65]
	v_fmac_f32_e32 v72, 0xba000000, v29
	v_mov_b32_e32 v78, v73
	v_mov_b32_e32 v79, v67
	v_mov_b32_e32 v73, v66
	v_pk_add_f32 v[64:65], v[64:65], v[64:65] op_sel_hi:[0,1]
	v_pk_mul_f32 v[68:69], v[78:79], v[78:79]
	v_pk_mul_f32 v[66:67], v[72:73], v[72:73]
	v_fmac_f32_e32 v34, 0xba000000, v29
	v_pk_mov_b32 v[70:71], v[66:67], v[68:69] op_sel:[1,0]
	v_mov_b32_e32 v67, v69
	v_fmac_f32_e32 v35, 0xba000000, v29
	v_fmac_f32_e32 v38, 0xba000000, v29
	v_mul_f32_e32 v64, v34, v34
	v_pk_add_f32 v[66:67], v[70:71], v[66:67]
	v_fmac_f32_e32 v39, 0xba000000, v29
	v_pk_fma_f32 v[68:69], v[34:35], v[34:35], v[64:65] op_sel_hi:[1,1,0]
	v_mul_f32_e32 v64, v38, v38
	v_pk_add_f32 v[66:67], v[66:67], v[66:67] op_sel_hi:[0,1]
	v_pk_fma_f32 v[70:71], v[38:39], v[38:39], v[64:65] op_sel_hi:[1,1,0]
	v_fmac_f32_e32 v30, 0xba000000, v29
	v_fmac_f32_e32 v28, 0xba000000, v29
	v_fmac_f32_e32 v36, 0xba000000, v29
	v_fmac_f32_e32 v32, 0xba000000, v29
	v_mul_f32_e32 v68, v32, v32
	v_mul_f32_e32 v70, v36, v36
	v_mul_f32_e32 v66, v28, v28
	v_mul_f32_e32 v64, v30, v30
	v_pk_add_f32 v[68:69], v[68:69], v[70:71]
	v_pk_add_f32 v[64:65], v[66:67], v[64:65]
	v_mov_b32_e32 v151, v60
	v_pk_add_f32 v[64:65], v[68:69], v[64:65]
	v_mov_b32_e32 v60, v59
	v_add_f32_e32 v29, v64, v65
	global_load_dwordx4 v[64:67], v[4:5], off
	global_load_dwordx4 v[68:71], v[6:7], off
	global_load_dwordx4 v[94:97], v[4:5], off offset:1024
	global_load_dwordx4 v[98:101], v[6:7], off offset:1024
	global_load_dwordx4 v[102:105], v[4:5], off offset:2048
	global_load_dwordx4 v[106:109], v[6:7], off offset:2048
	global_load_dwordx4 v[110:113], v[4:5], off offset:3072
	global_load_dwordx4 v[114:117], v[6:7], off offset:3072
	global_load_dwordx4 v[118:121], v[8:9], off
	global_load_dwordx4 v[122:125], v[10:11], off
	global_load_dwordx4 v[126:129], v[12:13], off
	global_load_dwordx4 v[130:133], v[14:15], off
	global_load_dwordx4 v[134:137], v[16:17], off
	global_load_dwordx4 v[138:141], v[18:19], off
	global_load_dwordx4 v[142:145], v[20:21], off
	global_load_dwordx4 v[146:149], v[22:23], off
	ds_bpermute_b32 v31, v82, v29
	v_mov_b32_e32 v59, v56
	v_mov_b32_e32 v56, v55
	v_mov_b32_e32 v150, v58
	v_mov_b32_e32 v58, v54
	s_waitcnt lgkmcnt(0)
	v_add_f32_e32 v29, v29, v31
	ds_bpermute_b32 v31, v83, v29
	s_waitcnt lgkmcnt(0)
	v_add_f32_e32 v29, v29, v31
	ds_bpermute_b32 v31, v84, v29
	s_waitcnt lgkmcnt(0)
	v_add_f32_e32 v29, v29, v31
	ds_bpermute_b32 v31, v85, v29
	s_waitcnt lgkmcnt(0)
	v_add_f32_e32 v29, v29, v31
	ds_bpermute_b32 v31, v86, v29
	s_waitcnt lgkmcnt(0)
	v_add_f32_e32 v29, v29, v31
	ds_bpermute_b32 v31, v87, v29
	s_waitcnt lgkmcnt(0)
	v_add_f32_e32 v29, v29, v31
	v_fmamk_f32 v29, v29, 0x3a000000, v89
	v_mul_f32_e32 v31, 0x4f800000, v29
	v_cmp_gt_f32_e32 vcc, s39, v29
	s_nop 1
	v_cndmask_b32_e32 v29, v29, v31, vcc
	v_sqrt_f32_e32 v31, v29
	s_nop 0
	v_add_u32_e32 v33, -1, v31
	v_fma_f32 v37, -v33, v31, v29
	v_cmp_ge_f32_e64 s[2:3], 0, v37
	v_add_u32_e32 v37, 1, v31
	s_nop 0
	v_cndmask_b32_e64 v33, v31, v33, s[2:3]
	v_fma_f32 v31, -v37, v31, v29
	v_cmp_lt_f32_e64 s[2:3], 0, v31
	s_nop 1
	v_cndmask_b32_e64 v31, v33, v37, s[2:3]
	v_mul_f32_e32 v33, 0x37800000, v31
	v_cndmask_b32_e32 v31, v31, v33, vcc
	v_cmp_class_f32_e32 vcc, v29, v90
	s_nop 1
	v_cndmask_b32_e32 v29, v31, v29, vcc
	v_div_scale_f32 v31, s[2:3], v29, v29, 1.0
	v_rcp_f32_e32 v33, v31
	s_mov_b32 s2, s18
	s_add_i32 s18, s18, 8
	s_cmp_ge_i32 s18, s34
	v_fma_f32 v37, -v31, v33, 1.0
	v_fmac_f32_e32 v33, v37, v33
	v_div_scale_f32 v37, vcc, 1.0, v29, 1.0
	v_mul_f32_e32 v41, v37, v33
	v_fma_f32 v43, -v31, v41, v37
	v_fmac_f32_e32 v41, v43, v33
	v_fma_f32 v31, -v31, v41, v37
	v_div_fmas_f32 v31, v31, v33, v41
	v_div_fixup_f32 v152, v31, v29, 1.0
	v_pk_mul_f32 v[54:55], v[60:61], v[152:153] op_sel_hi:[1,0]
	v_pk_mul_f32 v[56:57], v[56:57], v[152:153] op_sel_hi:[1,0]
	v_mov_b32_e32 v29, v30
	s_waitcnt vmcnt(14)
	v_pk_fma_f32 v[74:75], v[66:67], v[56:57], v[70:71]
	v_pk_fma_f32 v[76:77], v[64:65], v[54:55], v[68:69]
	v_pk_mul_f32 v[54:55], v[150:151], v[152:153] op_sel_hi:[1,0]
	v_pk_mul_f32 v[56:57], v[58:59], v[152:153] op_sel_hi:[1,0]
	v_pk_mul_f32 v[44:45], v[44:45], v[152:153] op_sel_hi:[1,0]
	v_pk_mul_f32 v[28:29], v[28:29], v[152:153] op_sel_hi:[1,0]
	s_waitcnt vmcnt(12)
	v_pk_fma_f32 v[66:67], v[96:97], v[56:57], v[100:101]
	v_pk_fma_f32 v[70:71], v[94:95], v[54:55], v[98:99]
	v_pk_mul_f32 v[52:53], v[52:53], v[152:153] op_sel_hi:[1,0]
	v_pk_mul_f32 v[54:55], v[62:63], v[152:153] op_sel_hi:[1,0]
	s_waitcnt vmcnt(8)
	v_pk_fma_f32 v[64:65], v[110:111], v[44:45], v[114:115]
	s_waitcnt vmcnt(0)
	v_pk_fma_f32 v[44:45], v[144:145], v[28:29], v[148:149]
	v_max_f32_e64 v28, |v76|, |v77|
	v_max_f32_e64 v29, |v74|, |v75|
	v_pk_fma_f32 v[62:63], v[104:105], v[54:55], v[108:109]
	v_pk_fma_f32 v[68:69], v[102:103], v[52:53], v[106:107]
	v_pk_mul_f32 v[46:47], v[46:47], v[152:153] op_sel_hi:[1,0]
	v_mov_b32_e32 v43, v50
	v_mov_b32_e32 v41, v48
	v_max3_f32 v28, v28, 0, v29
	v_max_f32_e64 v29, |v70|, |v71|
	v_max_f32_e64 v30, |v66|, |v67|
	v_pk_fma_f32 v[60:61], v[112:113], v[46:47], v[116:117]
	v_pk_mul_f32 v[42:43], v[42:43], v[152:153] op_sel_hi:[1,0]
	v_pk_mul_f32 v[40:41], v[40:41], v[152:153] op_sel_hi:[1,0]
	v_max3_f32 v28, v28, v29, v30
	v_max_f32_e64 v29, |v68|, |v69|
	v_max_f32_e64 v30, |v62|, |v63|
	v_pk_fma_f32 v[54:55], v[120:121], v[40:41], v[124:125]
	v_pk_fma_f32 v[58:59], v[118:119], v[42:43], v[122:123]
	v_pk_mul_f32 v[40:41], v[72:73], v[152:153] op_sel_hi:[1,0]
	v_pk_mul_f32 v[42:43], v[78:79], v[152:153] op_sel_hi:[1,0]
	v_max3_f32 v28, v28, v29, v30
	v_max_f32_e64 v29, |v64|, |v65|
	v_max_f32_e64 v30, |v60|, |v61|
	v_pk_fma_f32 v[52:53], v[128:129], v[42:43], v[132:133]
	v_pk_fma_f32 v[56:57], v[126:127], v[40:41], v[130:131]
	v_pk_mul_f32 v[34:35], v[34:35], v[152:153] op_sel_hi:[1,0]
	v_pk_mul_f32 v[38:39], v[38:39], v[152:153] op_sel_hi:[1,0]
	v_mov_b32_e32 v33, v36
	v_max3_f32 v28, v28, v29, v30
	v_max_f32_e64 v29, |v58|, |v59|
	v_max_f32_e64 v30, |v54|, |v55|
	v_pk_fma_f32 v[46:47], v[136:137], v[38:39], v[140:141]
	v_pk_fma_f32 v[50:51], v[134:135], v[34:35], v[138:139]
	v_pk_mul_f32 v[32:33], v[32:33], v[152:153] op_sel_hi:[1,0]
	v_max3_f32 v28, v28, v29, v30
	v_max_f32_e64 v29, |v56|, |v57|
	v_max_f32_e64 v30, |v52|, |v53|
	v_pk_fma_f32 v[48:49], v[142:143], v[32:33], v[146:147]
	v_max3_f32 v28, v28, v29, v30
	v_max_f32_e64 v29, |v50|, |v51|
	v_max_f32_e64 v30, |v46|, |v47|
	v_max3_f32 v28, v28, v29, v30
	v_max_f32_e64 v29, |v48|, |v49|
	v_max_f32_e64 v30, |v44|, |v45|
	v_max3_f32 v28, v28, v29, v30
	ds_bpermute_b32 v29, v82, v28
	s_cselect_b64 s[28:29], -1, 0
	s_cmp_lt_i32 s18, s34
	s_cselect_b32 s2, s18, s2
	s_ashr_i32 s3, s2, 31
	s_waitcnt lgkmcnt(0)
	v_max_f32_e32 v29, v29, v29
	v_max_f32_e32 v28, v28, v29
	ds_bpermute_b32 v29, v83, v28
	s_lshl_b64 s[2:3], s[2:3], 12
	v_lshl_add_u64 v[30:31], v[2:3], 0, s[2:3]
	s_waitcnt lgkmcnt(0)
	v_max_f32_e32 v29, v29, v29
	v_max_f32_e32 v28, v28, v29
	ds_bpermute_b32 v29, v84, v28
	s_waitcnt lgkmcnt(0)
	v_max_f32_e32 v29, v29, v29
	v_max_f32_e32 v28, v28, v29
	ds_bpermute_b32 v29, v85, v28
	s_waitcnt lgkmcnt(0)
	v_max_f32_e32 v29, v29, v29
	v_max_f32_e32 v28, v28, v29
	ds_bpermute_b32 v29, v86, v28
	s_waitcnt lgkmcnt(0)
	v_max_f32_e32 v29, v29, v29
	v_max_f32_e32 v32, v28, v29
	ds_bpermute_b32 v33, v87, v32
	global_load_dwordx2 v[36:37], v[30:31], off
	global_load_dwordx2 v[38:39], v[30:31], off offset:512
	global_load_dwordx2 v[40:41], v[30:31], off offset:1024
	global_load_dwordx2 v[28:29], v[30:31], off offset:1536
	s_waitcnt lgkmcnt(0)
	v_max_f32_e32 v33, v33, v33
	v_max_f32_e32 v72, v32, v33
	global_load_dwordx2 v[34:35], v[30:31], off offset:2048
	global_load_dwordx2 v[42:43], v[30:31], off offset:2560
	global_load_dwordx2 v[32:33], v[30:31], off offset:3072
	s_nop 0
	global_load_dwordx2 v[30:31], v[30:31], off offset:3584
	v_div_scale_f32 v73, s[2:3], v72, v72, s40
	v_rcp_f32_e32 v78, v73
	s_nop 0
	v_fma_f32 v79, -v73, v78, 1.0
	v_fmac_f32_e32 v78, v79, v78
	v_div_scale_f32 v79, vcc, s40, v72, s40
	v_mul_f32_e32 v94, v79, v78
	v_fma_f32 v95, -v73, v94, v79
	v_fmac_f32_e32 v94, v95, v78
	v_fma_f32 v73, -v73, v94, v79
	v_div_fmas_f32 v73, v73, v78, v94
	v_div_fixup_f32 v73, v73, v72, s40
	v_cmp_lt_f32_e32 vcc, 0, v72
	v_cvt_pk_bf16_f32 v78, v76, v77
	v_cvt_pk_bf16_f32 v79, v74, v75
	global_store_dwordx2 v[26:27], v[78:79], off offset:-2048 sc1
	s_nop 0
	v_cndmask_b32_e32 v73, 0, v73, vcc
	v_fmaak_f32 v78, v76, v73, 0x4b400000
	v_fmaak_f32 v79, v77, v73, 0x4b400000
	v_fmaak_f32 v94, v74, v73, 0x4b400000
	v_fmaak_f32 v95, v75, v73, 0x4b400000
	v_perm_b32 v78, v79, v78, s41
	v_perm_b32 v79, v95, v94, s42
	v_or_b32_e32 v78, v79, v78
	global_store_dword v[24:25], v78, off offset:-1024 sc1
	v_cvt_pk_bf16_f32 v78, v70, v71
	v_cvt_pk_bf16_f32 v79, v66, v67
	global_store_dwordx2 v[26:27], v[78:79], off offset:-1536 sc1
	v_fmaak_f32 v78, v70, v73, 0x4b400000
	v_fmaak_f32 v79, v71, v73, 0x4b400000
	v_fmaak_f32 v94, v66, v73, 0x4b400000
	v_fmaak_f32 v95, v67, v73, 0x4b400000
	v_perm_b32 v78, v79, v78, s41
	v_perm_b32 v79, v95, v94, s42
	v_or_b32_e32 v78, v79, v78
	global_store_dword v[24:25], v78, off offset:-768 sc1
	v_cvt_pk_bf16_f32 v78, v68, v69
	v_cvt_pk_bf16_f32 v79, v62, v63
	global_store_dwordx2 v[26:27], v[78:79], off offset:-1024 sc1
	v_fmaak_f32 v78, v68, v73, 0x4b400000
	v_fmaak_f32 v79, v69, v73, 0x4b400000
	v_fmaak_f32 v94, v62, v73, 0x4b400000
	v_fmaak_f32 v95, v63, v73, 0x4b400000
	v_perm_b32 v78, v79, v78, s41
	v_perm_b32 v79, v95, v94, s42
	v_or_b32_e32 v78, v79, v78
	global_store_dword v[24:25], v78, off offset:-512 sc1
	v_cvt_pk_bf16_f32 v78, v64, v65
	v_cvt_pk_bf16_f32 v79, v60, v61
	global_store_dwordx2 v[26:27], v[78:79], off offset:-512 sc1
	v_fmaak_f32 v78, v64, v73, 0x4b400000
	v_fmaak_f32 v79, v65, v73, 0x4b400000
	v_fmaak_f32 v94, v60, v73, 0x4b400000
	v_fmaak_f32 v95, v61, v73, 0x4b400000
	v_perm_b32 v78, v79, v78, s41
	v_perm_b32 v79, v95, v94, s42
	v_or_b32_e32 v78, v79, v78
	global_store_dword v[24:25], v78, off offset:-256 sc1
	v_cvt_pk_bf16_f32 v78, v58, v59
	v_cvt_pk_bf16_f32 v79, v54, v55
	global_store_dwordx2 v[26:27], v[78:79], off sc1
	v_fmaak_f32 v78, v58, v73, 0x4b400000
	v_fmaak_f32 v79, v59, v73, 0x4b400000
	v_fmaak_f32 v94, v54, v73, 0x4b400000
	v_fmaak_f32 v95, v55, v73, 0x4b400000
	v_perm_b32 v78, v79, v78, s41
	v_perm_b32 v79, v95, v94, s42
	v_or_b32_e32 v78, v79, v78
	global_store_dword v[24:25], v78, off sc1
	v_cvt_pk_bf16_f32 v78, v56, v57
	v_cvt_pk_bf16_f32 v79, v52, v53
	global_store_dwordx2 v[26:27], v[78:79], off offset:512 sc1
	v_fmaak_f32 v78, v56, v73, 0x4b400000
	v_fmaak_f32 v79, v57, v73, 0x4b400000
	v_fmaak_f32 v94, v52, v73, 0x4b400000
	v_fmaak_f32 v95, v53, v73, 0x4b400000
	v_perm_b32 v78, v79, v78, s41
	v_perm_b32 v79, v95, v94, s42
	v_or_b32_e32 v78, v79, v78
	global_store_dword v[24:25], v78, off offset:256 sc1
	v_cvt_pk_bf16_f32 v78, v50, v51
	v_cvt_pk_bf16_f32 v79, v46, v47
	global_store_dwordx2 v[26:27], v[78:79], off offset:1024 sc1
	v_fmaak_f32 v78, v50, v73, 0x4b400000
	v_fmaak_f32 v79, v51, v73, 0x4b400000
	v_fmaak_f32 v94, v46, v73, 0x4b400000
	v_fmaak_f32 v95, v47, v73, 0x4b400000
	v_perm_b32 v78, v79, v78, s41
	v_perm_b32 v79, v95, v94, s42
	v_or_b32_e32 v78, v79, v78
	global_store_dword v[24:25], v78, off offset:512 sc1
	v_cvt_pk_bf16_f32 v78, v48, v49
	v_cvt_pk_bf16_f32 v79, v44, v45
	global_store_dwordx2 v[26:27], v[78:79], off offset:1536 sc1
	v_fmaak_f32 v78, v48, v73, 0x4b400000
	v_fmaak_f32 v79, v49, v73, 0x4b400000
	v_fmaak_f32 v94, v44, v73, 0x4b400000
	v_fmaak_f32 v73, v45, v73, 0x4b400000
	v_perm_b32 v78, v79, v78, s41
	v_perm_b32 v73, v73, v94, s42
	v_or_b32_e32 v73, v73, v78
	global_store_dword v[24:25], v73, off offset:768 sc1
	s_and_saveexec_b64 s[2:3], s[0:1]
	s_cbranch_execz .LBB0_1696
	v_mul_f32_e32 v72, 0x3c010204, v72
	v_cndmask_b32_e32 v72, 1.0, v72, vcc
	global_store_dword v91, v72, s[22:23]

.LBB0_1775:
	s_or_b64 exec, exec, s[14:15]
	v_lshlrev_b64 v[24:25], 11, v[24:25]
	v_lshlrev_b64 v[22:23], 11, v[22:23]
	v_lshl_add_u64 v[24:25], v[18:19], 0, v[24:25]
	v_lshl_add_u64 v[22:23], v[18:19], 0, v[22:23]
	global_store_dwordx4 v[24:25], v[0:3], off sc1
	global_store_dwordx4 v[22:23], v[0:3], off sc1
	global_store_dwordx4 v[24:25], v[4:7], off offset:1024 sc1
	global_store_dwordx4 v[22:23], v[4:7], off offset:1024 sc1
	s_waitcnt vmcnt(5)
	v_mov_b64_e32 v[0:1], v[8:9]
	s_add_i32 s6, s6, s5
	s_waitcnt vmcnt(4)
	v_mov_b64_e32 v[4:5], v[12:13]
	s_andn2_b64 vcc, exec, s[8:9]
	v_mov_b64_e32 v[2:3], v[10:11]
	v_mov_b64_e32 v[6:7], v[14:15]
	s_mov_b64 s[12:13], s[10:11]
	v_mov_b64_e32 v[22:23], v[20:21]
	s_cbranch_vccz .LBB0_1780

.LBB0_1993:
	s_add_i32 s14, s24, s26
	s_cmpk_gt_i32 s14, 0x3fff
	s_cbranch_scc1 .LBB0_1992
	s_ashr_i32 s9, s8, 31
	s_lshl_b64 s[2:3], s[8:9], 2
	s_add_u32 s16, s20, s2
	s_addc_u32 s17, s21, s3
	global_load_dwordx2 v[26:27], v58, s[16:17]
	s_waitcnt vmcnt(0)
	v_readfirstlane_b32 s18, v26
	v_readfirstlane_b32 s16, v27
	s_max_i32 s9, s18, s16
	s_cmp_ge_i32 s9, s27
	s_cbranch_scc1 .LBB0_1992
	s_ashr_i32 s15, s14, 31
	s_add_u32 s2, s11, s2
	s_addc_u32 s3, s13, s3
	s_lshl_b64 s[34:35], s[14:15], 12
	v_lshl_add_u64 v[28:29], v[22:23], 0, s[34:35]
	global_load_dwordx2 v[26:27], v[28:29], off
	global_load_dwordx2 v[30:31], v[28:29], off offset:512
	global_load_dwordx2 v[32:33], v[28:29], off offset:1024
	s_ashr_i32 s19, s18, 31
	s_ashr_i32 s17, s16, 31
	s_lshl_b64 s[18:19], s[18:19], 12
	s_lshl_b64 s[16:17], s[16:17], 12
	v_lshl_add_u64 v[34:35], v[24:25], 0, s[18:19]
	v_lshl_add_u64 v[38:39], v[24:25], 0, s[16:17]
	global_load_dwordx2 v[36:37], v[34:35], off
	global_load_dwordx2 v[40:41], v[38:39], off
	global_load_dwordx2 v[42:43], v[34:35], off offset:512
	global_load_dwordx2 v[44:45], v[38:39], off offset:512
	global_load_dwordx2 v[46:47], v[34:35], off offset:1024
	global_load_dwordx2 v[48:49], v[38:39], off offset:1024
	global_load_dwordx2 v[56:57], v58, s[2:3]
	global_load_dwordx2 v[50:51], v[28:29], off offset:1536
	global_load_dwordx2 v[52:53], v[34:35], off offset:1536
	global_load_dwordx2 v[54:55], v[38:39], off offset:1536
	global_load_dwordx2 v[70:71], v[28:29], off offset:2048
	global_load_dwordx2 v[72:73], v[28:29], off offset:2560
	global_load_dwordx2 v[74:75], v[28:29], off offset:3072
	global_load_dwordx2 v[76:77], v[34:35], off offset:2048
	global_load_dwordx2 v[78:79], v[34:35], off offset:2560
	global_load_dwordx2 v[80:81], v[34:35], off offset:3072
	global_load_dwordx2 v[82:83], v[38:39], off offset:2048
	global_load_dwordx2 v[84:85], v[38:39], off offset:2560
	global_load_dwordx2 v[86:87], v[38:39], off offset:3072
	global_load_dwordx2 v[88:89], v[28:29], off offset:3584
	global_load_dwordx2 v[90:91], v[34:35], off offset:3584
	v_cmp_lt_i32_e32 vcc, v64, v63
	s_waitcnt vmcnt(19)
	v_lshlrev_b32_e32 v96, 16, v40
	s_waitcnt vmcnt(18)
	v_lshlrev_b32_e32 v98, 16, v42
	v_and_b32_e32 v99, 0xffff0000, v42
	v_lshlrev_b32_e32 v42, 16, v43
	v_and_b32_e32 v43, 0xffff0000, v43
	s_waitcnt vmcnt(16)
	v_lshlrev_b32_e32 v102, 16, v46
	v_and_b32_e32 v103, 0xffff0000, v46
	s_waitcnt vmcnt(14)
	v_pk_mul_f32 v[42:43], v[56:57], v[42:43] op_sel_hi:[0,1]
	v_pk_mul_f32 v[102:103], v[56:57], v[102:103] op_sel_hi:[0,1]
	v_and_b32_e32 v97, 0xffff0000, v40
	v_lshlrev_b32_e32 v28, 16, v26
	v_lshlrev_b32_e32 v34, 16, v30
	v_and_b32_e32 v35, 0xffff0000, v30
	v_lshlrev_b32_e32 v30, 16, v31
	v_and_b32_e32 v31, 0xffff0000, v31
	v_lshlrev_b32_e32 v92, 16, v32
	v_and_b32_e32 v93, 0xffff0000, v32
	v_pk_fma_f32 v[30:31], v[30:31], s[12:13], v[42:43] op_sel_hi:[1,0,1]
	v_pk_fma_f32 v[42:43], v[92:93], s[12:13], v[102:103] op_sel_hi:[1,0,1]
	global_load_dwordx2 v[92:93], v[38:39], off offset:3584
	v_lshlrev_b32_e32 v94, 16, v36
	v_and_b32_e32 v95, 0xffff0000, v36
	v_and_b32_e32 v29, 0xffff0000, v26
	v_lshlrev_b32_e32 v36, 16, v37
	v_and_b32_e32 v37, 0xffff0000, v37
	v_pk_mul_f32 v[94:95], v[56:57], v[94:95] op_sel_hi:[0,1]
	v_lshlrev_b32_e32 v26, 16, v27
	v_and_b32_e32 v27, 0xffff0000, v27
	v_lshlrev_b32_e32 v100, 16, v44
	v_and_b32_e32 v101, 0xffff0000, v44
	v_lshlrev_b32_e32 v44, 16, v45
	v_and_b32_e32 v45, 0xffff0000, v45
	v_lshlrev_b32_e32 v46, 16, v47
	v_and_b32_e32 v47, 0xffff0000, v47
	v_lshlrev_b32_e32 v104, 16, v48
	v_and_b32_e32 v105, 0xffff0000, v48
	v_pk_mul_f32 v[36:37], v[56:57], v[36:37] op_sel_hi:[0,1]
	v_pk_fma_f32 v[28:29], v[28:29], s[12:13], v[94:95] op_sel_hi:[1,0,1]
	v_lshlrev_b32_e32 v32, 16, v33
	v_and_b32_e32 v33, 0xffff0000, v33
	v_lshlrev_b32_e32 v40, 16, v41
	v_and_b32_e32 v41, 0xffff0000, v41
	v_pk_mul_f32 v[46:47], v[56:57], v[46:47] op_sel_hi:[0,1]
	v_pk_fma_f32 v[26:27], v[26:27], s[12:13], v[36:37] op_sel_hi:[1,0,1]
	v_pk_fma_f32 v[36:37], v[56:57], v[96:97], v[28:29] op_sel:[1,0,0]
	v_pk_fma_f32 v[30:31], v[56:57], v[44:45], v[30:31] op_sel:[1,0,0]
	v_pk_fma_f32 v[28:29], v[56:57], v[104:105], v[42:43] op_sel:[1,0,0]
	s_waitcnt vmcnt(13)
	v_lshlrev_b32_e32 v42, 16, v52
	v_and_b32_e32 v43, 0xffff0000, v52
	v_lshlrev_b32_e32 v44, 16, v53
	v_and_b32_e32 v45, 0xffff0000, v53
	v_lshlrev_b32_e32 v48, 16, v49
	v_and_b32_e32 v49, 0xffff0000, v49
	v_pk_fma_f32 v[46:47], v[32:33], s[12:13], v[46:47] op_sel_hi:[1,0,1]
	v_pk_fma_f32 v[32:33], v[56:57], v[40:41], v[26:27] op_sel:[1,0,0]
	v_lshlrev_b32_e32 v40, 16, v50
	v_and_b32_e32 v41, 0xffff0000, v50
	v_lshlrev_b32_e32 v38, 16, v51
	v_and_b32_e32 v39, 0xffff0000, v51
	v_pk_mul_f32 v[44:45], v[56:57], v[44:45] op_sel_hi:[0,1]
	v_pk_mul_f32 v[42:43], v[56:57], v[42:43] op_sel_hi:[0,1]
	v_pk_fma_f32 v[26:27], v[56:57], v[48:49], v[46:47] op_sel:[1,0,0]
	s_waitcnt vmcnt(12)
	v_lshlrev_b32_e32 v46, 16, v54
	v_and_b32_e32 v47, 0xffff0000, v54
	v_lshlrev_b32_e32 v48, 16, v55
	v_and_b32_e32 v49, 0xffff0000, v55
	v_pk_fma_f32 v[40:41], v[40:41], s[12:13], v[42:43] op_sel_hi:[1,0,1]
	v_pk_fma_f32 v[38:39], v[38:39], s[12:13], v[44:45] op_sel_hi:[1,0,1]
	v_pk_fma_f32 v[40:41], v[56:57], v[46:47], v[40:41] op_sel:[1,0,0]
	v_pk_fma_f32 v[38:39], v[56:57], v[48:49], v[38:39] op_sel:[1,0,0]
	s_waitcnt vmcnt(8)
	v_lshlrev_b32_e32 v46, 16, v76
	v_and_b32_e32 v47, 0xffff0000, v76
	v_lshlrev_b32_e32 v48, 16, v77
	v_and_b32_e32 v49, 0xffff0000, v77
	v_lshlrev_b32_e32 v42, 16, v70
	v_and_b32_e32 v43, 0xffff0000, v70
	v_lshlrev_b32_e32 v44, 16, v71
	v_and_b32_e32 v45, 0xffff0000, v71
	v_pk_mul_f32 v[48:49], v[56:57], v[48:49] op_sel_hi:[0,1]
	v_pk_mul_f32 v[46:47], v[56:57], v[46:47] op_sel_hi:[0,1]
	s_waitcnt vmcnt(5)
	v_lshlrev_b32_e32 v50, 16, v82
	v_and_b32_e32 v51, 0xffff0000, v82
	v_lshlrev_b32_e32 v52, 16, v83
	v_and_b32_e32 v53, 0xffff0000, v83
	v_pk_fma_f32 v[46:47], v[42:43], s[12:13], v[46:47] op_sel_hi:[1,0,1]
	v_pk_fma_f32 v[42:43], v[44:45], s[12:13], v[48:49] op_sel_hi:[1,0,1]
	v_pk_fma_f32 v[44:45], v[56:57], v[50:51], v[46:47] op_sel:[1,0,0]
	v_pk_fma_f32 v[42:43], v[56:57], v[52:53], v[42:43] op_sel:[1,0,0]
	v_lshlrev_b32_e32 v50, 16, v78
	v_and_b32_e32 v51, 0xffff0000, v78
	v_lshlrev_b32_e32 v52, 16, v79
	v_and_b32_e32 v53, 0xffff0000, v79
	v_lshlrev_b32_e32 v46, 16, v72
	v_and_b32_e32 v47, 0xffff0000, v72
	v_lshlrev_b32_e32 v48, 16, v73
	v_and_b32_e32 v49, 0xffff0000, v73
	v_pk_mul_f32 v[52:53], v[56:57], v[52:53] op_sel_hi:[0,1]
	v_pk_mul_f32 v[50:51], v[56:57], v[50:51] op_sel_hi:[0,1]
	s_waitcnt vmcnt(4)
	v_lshlrev_b32_e32 v54, 16, v84
	v_and_b32_e32 v55, 0xffff0000, v84
	v_lshlrev_b32_e32 v70, 16, v85
	v_and_b32_e32 v71, 0xffff0000, v85
	v_pk_fma_f32 v[50:51], v[46:47], s[12:13], v[50:51] op_sel_hi:[1,0,1]
	v_pk_fma_f32 v[46:47], v[48:49], s[12:13], v[52:53] op_sel_hi:[1,0,1]
	v_pk_fma_f32 v[48:49], v[56:57], v[54:55], v[50:51] op_sel:[1,0,0]
	v_pk_fma_f32 v[46:47], v[56:57], v[70:71], v[46:47] op_sel:[1,0,0]
	v_lshlrev_b32_e32 v54, 16, v80
	v_and_b32_e32 v55, 0xffff0000, v80
	v_lshlrev_b32_e32 v70, 16, v81
	v_and_b32_e32 v71, 0xffff0000, v81
	v_lshlrev_b32_e32 v50, 16, v74
	v_and_b32_e32 v51, 0xffff0000, v74
	v_lshlrev_b32_e32 v52, 16, v75
	v_and_b32_e32 v53, 0xffff0000, v75
	v_pk_mul_f32 v[70:71], v[56:57], v[70:71] op_sel_hi:[0,1]
	v_pk_mul_f32 v[54:55], v[56:57], v[54:55] op_sel_hi:[0,1]
	s_waitcnt vmcnt(3)
	v_lshlrev_b32_e32 v72, 16, v86
	v_and_b32_e32 v73, 0xffff0000, v86
	v_lshlrev_b32_e32 v74, 16, v87
	v_and_b32_e32 v75, 0xffff0000, v87
	v_pk_fma_f32 v[54:55], v[50:51], s[12:13], v[54:55] op_sel_hi:[1,0,1]
	v_pk_fma_f32 v[50:51], v[52:53], s[12:13], v[70:71] op_sel_hi:[1,0,1]
	v_pk_mul_f32 v[98:99], v[56:57], v[98:99] op_sel_hi:[0,1]
	v_pk_fma_f32 v[50:51], v[56:57], v[74:75], v[50:51] op_sel:[1,0,0]
	v_pk_fma_f32 v[52:53], v[56:57], v[72:73], v[54:55] op_sel:[1,0,0]
	s_waitcnt vmcnt(1)
	v_lshlrev_b32_e32 v72, 16, v90
	v_and_b32_e32 v73, 0xffff0000, v90
	v_lshlrev_b32_e32 v74, 16, v91
	v_and_b32_e32 v75, 0xffff0000, v91
	v_pk_fma_f32 v[34:35], v[34:35], s[12:13], v[98:99] op_sel_hi:[1,0,1]
	v_lshlrev_b32_e32 v54, 16, v88
	v_and_b32_e32 v55, 0xffff0000, v88
	v_lshlrev_b32_e32 v70, 16, v89
	v_and_b32_e32 v71, 0xffff0000, v89
	v_pk_mul_f32 v[74:75], v[56:57], v[74:75] op_sel_hi:[0,1]
	v_pk_mul_f32 v[72:73], v[56:57], v[72:73] op_sel_hi:[0,1]
	v_pk_fma_f32 v[34:35], v[56:57], v[100:101], v[34:35] op_sel:[1,0,0]
	s_waitcnt vmcnt(0)
	v_lshlrev_b32_e32 v76, 16, v92
	v_and_b32_e32 v77, 0xffff0000, v92
	v_lshlrev_b32_e32 v78, 16, v93
	v_and_b32_e32 v79, 0xffff0000, v93
	v_pk_fma_f32 v[72:73], v[54:55], s[12:13], v[72:73] op_sel_hi:[1,0,1]
	v_pk_fma_f32 v[54:55], v[70:71], s[12:13], v[74:75] op_sel_hi:[1,0,1]
	v_mov_b32_e32 v70, v36
	v_pk_fma_f32 v[54:55], v[56:57], v[78:79], v[54:55] op_sel:[1,0,0]
	v_pk_fma_f32 v[56:57], v[56:57], v[76:77], v[72:73] op_sel:[1,0,0]
	v_mov_b32_e32 v71, v34
	v_mov_b32_e32 v72, v37
	v_mov_b32_e32 v73, v35
	v_pk_add_f32 v[70:71], v[70:71], v[72:73]
	v_mov_b32_e32 v72, v32
	v_mov_b32_e32 v73, v30
	v_mov_b32_e32 v74, v33
	v_mov_b32_e32 v75, v31
	v_pk_add_f32 v[72:73], v[72:73], v[74:75]
	v_mov_b32_e32 v74, v28
	v_pk_add_f32 v[70:71], v[70:71], v[72:73]
	v_pk_mov_b32 v[72:73], v[28:29], v[26:27] op_sel:[1,0]
	v_mov_b32_e32 v75, v27
	v_pk_add_f32 v[72:73], v[72:73], v[74:75]
	v_add_f32_e32 v70, 0, v70
	v_pk_add_f32 v[72:73], v[72:73], v[72:73] op_sel:[0,1] op_sel_hi:[1,0]
	v_add_f32_e32 v70, v70, v71
	v_add_f32_e32 v74, v40, v41
	v_add_f32_e32 v76, v38, v39
	v_mov_b32_e32 v71, v44
	v_mov_b32_e32 v73, v45
	v_mov_b32_e32 v75, v42
	v_mov_b32_e32 v77, v43
	v_pk_add_f32 v[70:71], v[70:71], v[72:73]
	v_pk_add_f32 v[72:73], v[74:75], v[76:77]
	v_mov_b32_e32 v74, v48
	v_pk_add_f32 v[70:71], v[70:71], v[72:73]
	v_pk_mov_b32 v[72:73], v[48:49], v[46:47] op_sel:[1,0]
	v_mov_b32_e32 v75, v47
	v_pk_add_f32 v[72:73], v[72:73], v[74:75]
	v_pk_add_f32 v[70:71], v[70:71], v[70:71] op_sel:[0,1] op_sel_hi:[1,0]
	v_pk_add_f32 v[72:73], v[72:73], v[72:73] op_sel:[0,1] op_sel_hi:[1,0]
	v_add_f32_e32 v74, v52, v53
	v_add_f32_e32 v76, v50, v51
	v_mov_b32_e32 v71, v56
	v_mov_b32_e32 v73, v57
	v_mov_b32_e32 v75, v54
	v_mov_b32_e32 v77, v55
	v_pk_add_f32 v[70:71], v[70:71], v[72:73]
	v_pk_add_f32 v[72:73], v[74:75], v[76:77]
	s_nop 0
	v_pk_add_f32 v[70:71], v[70:71], v[72:73]
	s_nop 0
	v_add_f32_e32 v70, v70, v71
	v_cndmask_b32_e32 v71, v62, v64, vcc
	v_lshlrev_b32_e32 v78, 2, v71
	ds_bpermute_b32 v71, v78, v70
	v_cmp_lt_i32_e32 vcc, v65, v63
	s_waitcnt lgkmcnt(0)
	v_add_f32_e32 v70, v70, v71
	v_cndmask_b32_e32 v71, v62, v65, vcc
	v_lshlrev_b32_e32 v86, 2, v71
	ds_bpermute_b32 v71, v86, v70
	v_cmp_lt_i32_e32 vcc, v66, v63
	s_waitcnt lgkmcnt(0)
	v_add_f32_e32 v70, v70, v71
	v_cndmask_b32_e32 v71, v62, v66, vcc
	v_lshlrev_b32_e32 v102, 2, v71
	ds_bpermute_b32 v71, v102, v70
	v_cmp_lt_i32_e32 vcc, v67, v63
	s_waitcnt lgkmcnt(0)
	v_add_f32_e32 v70, v70, v71
	v_cndmask_b32_e32 v71, v62, v67, vcc
	v_lshlrev_b32_e32 v118, 2, v71
	ds_bpermute_b32 v71, v118, v70
	v_cmp_lt_i32_e32 vcc, v68, v63
	s_waitcnt lgkmcnt(0)
	v_add_f32_e32 v70, v70, v71
	v_cndmask_b32_e32 v71, v62, v68, vcc
	v_lshlrev_b32_e32 v134, 2, v71
	ds_bpermute_b32 v71, v134, v70
	v_cmp_lt_i32_e32 vcc, v69, v63
	s_waitcnt lgkmcnt(0)
	v_add_f32_e32 v70, v70, v71
	v_cndmask_b32_e32 v71, v62, v69, vcc
	v_lshlrev_b32_e32 v135, 2, v71
	ds_bpermute_b32 v71, v135, v70
	s_waitcnt lgkmcnt(0)
	v_add_f32_e32 v79, v70, v71
	v_fmamk_f32 v37, v79, 0xba000000, v37
	v_fmamk_f32 v35, v79, 0xba000000, v35
	v_fmamk_f32 v33, v79, 0xba000000, v33
	v_fmac_f32_e32 v36, 0xba000000, v79
	v_fmamk_f32 v31, v79, 0xba000000, v31
	v_fmac_f32_e32 v34, 0xba000000, v79
	v_mov_b32_e32 v72, v37
	v_mov_b32_e32 v73, v35
	v_fmac_f32_e32 v32, 0xba000000, v79
	v_fmac_f32_e32 v30, 0xba000000, v79
	v_mov_b32_e32 v70, v36
	v_mov_b32_e32 v71, v34
	v_pk_mul_f32 v[72:73], v[72:73], v[72:73]
	v_mov_b32_e32 v74, v33
	v_mov_b32_e32 v75, v31
	v_pk_fma_f32 v[70:71], v[70:71], v[70:71], v[72:73]
	v_mov_b32_e32 v72, v32
	v_mov_b32_e32 v73, v30
	v_pk_mul_f32 v[74:75], v[74:75], v[74:75]
	v_fmamk_f32 v29, v79, 0xba000000, v29
	v_pk_fma_f32 v[72:73], v[72:73], v[72:73], v[74:75]
	v_fmac_f32_e32 v28, 0xba000000, v79
	v_pk_add_f32 v[70:71], v[70:71], v[72:73]
	v_fmamk_f32 v27, v79, 0xba000000, v27
	v_fmac_f32_e32 v26, 0xba000000, v79
	v_pk_add_f32 v[70:71], v[70:71], v[70:71] op_sel_hi:[0,1]
	v_pk_mul_f32 v[72:73], v[26:27], v[26:27]
	v_pk_mul_f32 v[74:75], v[28:29], v[28:29]
	v_fmac_f32_e32 v40, 0xba000000, v79
	v_pk_mov_b32 v[76:77], v[74:75], v[72:73] op_sel:[1,0]
	v_mov_b32_e32 v75, v73
	v_fmamk_f32 v41, v79, 0xba000000, v41
	v_fmac_f32_e32 v38, 0xba000000, v79
	v_mul_f32_e32 v70, v40, v40
	v_pk_add_f32 v[72:73], v[76:77], v[74:75]
	v_fmamk_f32 v39, v79, 0xba000000, v39
	v_pk_fma_f32 v[74:75], v[40:41], v[40:41], v[70:71] op_sel_hi:[1,1,0]
	v_mul_f32_e32 v70, v38, v38
	v_pk_add_f32 v[72:73], v[72:73], v[72:73] op_sel_hi:[0,1]
	v_pk_fma_f32 v[76:77], v[38:39], v[38:39], v[70:71] op_sel_hi:[1,1,0]
	v_fmamk_f32 v43, v79, 0xba000000, v43
	v_fmac_f32_e32 v42, 0xba000000, v79
	v_fmamk_f32 v45, v79, 0xba000000, v45
	v_fmac_f32_e32 v44, 0xba000000, v79
	v_mul_f32_e32 v74, v44, v44
	v_mul_f32_e32 v76, v45, v45
	v_mul_f32_e32 v72, v42, v42
	v_mul_f32_e32 v70, v43, v43
	v_pk_add_f32 v[74:75], v[74:75], v[76:77]
	v_pk_add_f32 v[70:71], v[72:73], v[70:71]
	v_fmamk_f32 v49, v79, 0xba000000, v49
	v_pk_add_f32 v[70:71], v[74:75], v[70:71]
	v_fmac_f32_e32 v48, 0xba000000, v79
	v_fmamk_f32 v47, v79, 0xba000000, v47
	v_fmac_f32_e32 v46, 0xba000000, v79
	v_pk_add_f32 v[70:71], v[70:71], v[70:71] op_sel_hi:[0,1]
	v_pk_mul_f32 v[72:73], v[46:47], v[46:47]
	v_pk_mul_f32 v[74:75], v[48:49], v[48:49]
	v_fmac_f32_e32 v52, 0xba000000, v79
	v_pk_mov_b32 v[76:77], v[74:75], v[72:73] op_sel:[1,0]
	v_mov_b32_e32 v75, v73
	v_fmamk_f32 v53, v79, 0xba000000, v53
	v_fmac_f32_e32 v50, 0xba000000, v79
	v_mul_f32_e32 v70, v52, v52
	v_pk_add_f32 v[72:73], v[76:77], v[74:75]
	v_fmamk_f32 v51, v79, 0xba000000, v51
	v_pk_fma_f32 v[74:75], v[52:53], v[52:53], v[70:71] op_sel_hi:[1,1,0]
	v_mul_f32_e32 v70, v50, v50
	v_pk_add_f32 v[72:73], v[72:73], v[72:73] op_sel_hi:[0,1]
	v_pk_fma_f32 v[76:77], v[50:51], v[50:51], v[70:71] op_sel_hi:[1,1,0]
	v_fmamk_f32 v55, v79, 0xba000000, v55
	v_fmac_f32_e32 v54, 0xba000000, v79
	v_fmamk_f32 v57, v79, 0xba000000, v57
	v_fmac_f32_e32 v56, 0xba000000, v79
	v_mul_f32_e32 v74, v56, v56
	v_mul_f32_e32 v76, v57, v57
	v_mul_f32_e32 v72, v54, v54
	v_mul_f32_e32 v70, v55, v55
	v_pk_add_f32 v[74:75], v[74:75], v[76:77]
	v_pk_add_f32 v[70:71], v[72:73], v[70:71]
	s_nop 0
	v_pk_add_f32 v[70:71], v[74:75], v[70:71]
	s_nop 0
	v_add_f32_e32 v79, v70, v71
	ds_bpermute_b32 v78, v78, v79
	global_load_dwordx4 v[70:73], v[2:3], off
	global_load_dwordx4 v[74:77], v[4:5], off
	s_waitcnt lgkmcnt(0)
	v_add_f32_e32 v94, v79, v78
	ds_bpermute_b32 v95, v86, v94
	global_load_dwordx4 v[78:81], v[2:3], off offset:1024
	global_load_dwordx4 v[82:85], v[4:5], off offset:1024
	global_load_dwordx4 v[86:89], v[2:3], off offset:2048
	global_load_dwordx4 v[90:93], v[4:5], off offset:2048
	s_waitcnt lgkmcnt(0)
	v_add_f32_e32 v110, v94, v95
	ds_bpermute_b32 v111, v102, v110
	global_load_dwordx4 v[94:97], v[2:3], off offset:3072
	global_load_dwordx4 v[98:101], v[4:5], off offset:3072
	global_load_dwordx4 v[102:105], v[6:7], off
	global_load_dwordx4 v[106:109], v[8:9], off
	s_waitcnt lgkmcnt(0)
	v_add_f32_e32 v126, v110, v111
	ds_bpermute_b32 v127, v118, v126
	global_load_dwordx4 v[110:113], v[10:11], off
	global_load_dwordx4 v[114:117], v[12:13], off
	global_load_dwordx4 v[118:121], v[14:15], off
	global_load_dwordx4 v[122:125], v[16:17], off
	s_waitcnt lgkmcnt(0)
	v_add_f32_e32 v136, v126, v127
	global_load_dwordx4 v[126:129], v[18:19], off
	global_load_dwordx4 v[130:133], v[20:21], off
	ds_bpermute_b32 v134, v134, v136
	s_waitcnt lgkmcnt(0)
	v_add_f32_e32 v134, v136, v134
	ds_bpermute_b32 v135, v135, v134
	s_waitcnt lgkmcnt(0)
	v_add_f32_e32 v134, v134, v135
	v_fmamk_f32 v134, v134, 0x3a000000, v59
	v_mul_f32_e32 v135, 0x4f800000, v134
	v_cmp_gt_f32_e32 vcc, s29, v134
	s_nop 1
	v_cndmask_b32_e32 v134, v134, v135, vcc
	v_sqrt_f32_e32 v135, v134
	s_nop 0
	v_add_u32_e32 v136, -1, v135
	v_fma_f32 v137, -v136, v135, v134
	v_cmp_ge_f32_e64 s[2:3], 0, v137
	v_add_u32_e32 v137, 1, v135
	s_nop 0
	v_cndmask_b32_e64 v136, v135, v136, s[2:3]
	v_fma_f32 v135, -v137, v135, v134
	v_cmp_lt_f32_e64 s[2:3], 0, v135
	s_nop 1
	v_cndmask_b32_e64 v135, v136, v137, s[2:3]
	v_mul_f32_e32 v136, 0x37800000, v135
	v_cndmask_b32_e32 v135, v135, v136, vcc
	v_cmp_class_f32_e32 vcc, v134, v60
	s_nop 1
	v_cndmask_b32_e32 v134, v135, v134, vcc
	v_div_scale_f32 v135, s[2:3], v134, v134, 1.0
	v_rcp_f32_e32 v136, v135
	s_lshl_b64 s[2:3], s[14:15], 13
	s_add_u32 s2, s64, s2
	s_addc_u32 s3, s65, s3
	v_fma_f32 v137, -v135, v136, 1.0
	v_fmac_f32_e32 v136, v137, v136
	v_div_scale_f32 v137, vcc, 1.0, v134, 1.0
	v_mul_f32_e32 v138, v137, v136
	v_fma_f32 v139, -v135, v138, v137
	v_fmac_f32_e32 v138, v139, v136
	v_fma_f32 v135, -v135, v138, v137
	v_div_fmas_f32 v135, v135, v136, v138
	v_div_fixup_f32 v134, v135, v134, 1.0
	v_pk_mul_f32 v[32:33], v[32:33], v[134:135] op_sel_hi:[1,0]
	v_pk_mul_f32 v[34:35], v[34:35], v[134:135] op_sel_hi:[1,0]
	v_pk_mul_f32 v[30:31], v[30:31], v[134:135] op_sel_hi:[1,0]
	v_pk_mul_f32 v[36:37], v[36:37], v[134:135] op_sel_hi:[1,0]
	s_waitcnt vmcnt(14)
	v_pk_fma_f32 v[72:73], v[72:73], v[32:33], v[76:77]
	v_pk_mul_f32 v[26:27], v[26:27], v[134:135] op_sel_hi:[1,0]
	v_pk_fma_f32 v[70:71], v[70:71], v[36:37], v[74:75]
	s_waitcnt vmcnt(12)
	v_pk_fma_f32 v[32:33], v[80:81], v[30:31], v[84:85]
	v_pk_fma_f32 v[30:31], v[78:79], v[34:35], v[82:83]
	v_pk_mul_f32 v[34:35], v[28:29], v[134:135] op_sel_hi:[1,0]
	s_waitcnt vmcnt(10)
	v_pk_fma_f32 v[28:29], v[88:89], v[26:27], v[92:93]
	v_pk_fma_f32 v[26:27], v[86:87], v[34:35], v[90:91]
	v_pk_mul_f32 v[34:35], v[40:41], v[134:135] op_sel_hi:[1,0]
	v_pk_mul_f32 v[36:37], v[38:39], v[134:135] op_sel_hi:[1,0]
	v_pk_mul_f32 v[38:39], v[44:45], v[134:135] op_sel_hi:[1,0]
	v_pk_mul_f32 v[44:45], v[46:47], v[134:135] op_sel_hi:[1,0]
	v_pk_mul_f32 v[46:47], v[52:53], v[134:135] op_sel_hi:[1,0]
	v_pk_mul_f32 v[52:53], v[54:55], v[134:135] op_sel_hi:[1,0]
	v_lshl_add_u64 v[54:55], v[0:1], 2, s[2:3]
	s_waitcnt vmcnt(8)
	v_pk_fma_f32 v[36:37], v[96:97], v[36:37], v[100:101]
	v_pk_fma_f32 v[34:35], v[94:95], v[34:35], v[98:99]
	v_pk_mul_f32 v[40:41], v[42:43], v[134:135] op_sel_hi:[1,0]
	global_store_dwordx4 v[54:55], v[70:73], off sc1
	global_store_dwordx4 v[54:55], v[30:33], off offset:1024 sc1
	global_store_dwordx4 v[54:55], v[26:29], off offset:2048 sc1
	global_store_dwordx4 v[54:55], v[34:37], off offset:3072 sc1
	s_waitcnt vmcnt(10)
	v_pk_fma_f32 v[40:41], v[104:105], v[40:41], v[108:109]
	v_add_co_u32_e32 v26, vcc, s30, v54
	v_pk_fma_f32 v[38:39], v[102:103], v[38:39], v[106:107]
	v_pk_mul_f32 v[42:43], v[48:49], v[134:135] op_sel_hi:[1,0]
	v_pk_mul_f32 v[48:49], v[50:51], v[134:135] op_sel_hi:[1,0]
	v_pk_mul_f32 v[50:51], v[56:57], v[134:135] op_sel_hi:[1,0]
	v_addc_co_u32_e32 v27, vcc, 0, v55, vcc
	s_waitcnt vmcnt(8)
	v_pk_fma_f32 v[44:45], v[112:113], v[44:45], v[116:117]
	v_pk_fma_f32 v[42:43], v[110:111], v[42:43], v[114:115]
	s_waitcnt vmcnt(6)
	v_pk_fma_f32 v[48:49], v[120:121], v[48:49], v[124:125]
	v_pk_fma_f32 v[46:47], v[118:119], v[46:47], v[122:123]
	s_waitcnt vmcnt(4)
	v_pk_fma_f32 v[52:53], v[128:129], v[52:53], v[132:133]
	v_pk_fma_f32 v[50:51], v[126:127], v[50:51], v[130:131]
	global_store_dwordx4 v[26:27], v[38:41], off sc1
	global_store_dwordx4 v[26:27], v[42:45], off offset:1024 sc1
	global_store_dwordx4 v[26:27], v[46:49], off offset:2048 sc1
	global_store_dwordx4 v[26:27], v[50:53], off offset:3072 sc1
	s_and_saveexec_b64 s[2:3], s[0:1]
	s_cbranch_execz .LBB0_1991
	s_lshl_b64 s[14:15], s[14:15], 2
	s_add_u32 s14, s22, s14
	s_addc_u32 s15, s23, s15
	global_store_dword v58, v61, s[14:15]
	s_branch .LBB0_1991

.LBB0_2073:
	s_abs_i32 s1, s15
	s_mul_hi_u32 s4, s1, s20
	s_mul_i32 s4, s4, s19
	s_sub_i32 s1, s1, s4
	s_ashr_i32 s0, s15, 31
	s_sub_i32 s4, s1, s19
	s_cmp_ge_u32 s1, s19
	s_cselect_b32 s1, s4, s1
	s_sub_i32 s4, s1, s19
	s_cmp_ge_u32 s1, s19
	s_cselect_b32 s1, s4, s1
	s_xor_b32 s1, s1, s0
	s_sub_i32 s0, s1, s0
	s_add_i32 s4, s18, s0
	s_cmpk_gt_i32 s4, 0x3fff
	s_cbranch_scc1 .LBB0_2072
	s_lshl_b32 s0, s4, 1
	s_ashr_i32 s1, s0, 31
	s_lshl_b64 s[0:1], s[0:1], 2
	s_add_u32 s6, s11, s0
	s_addc_u32 s7, s12, s1
	s_ashr_i32 s5, s4, 31
	s_lshl_b64 s[8:9], s[4:5], 2
	s_add_u32 s8, s13, s8
	s_addc_u32 s9, s14, s9
	global_load_dwordx2 v[26:27], v58, s[6:7]
	global_load_dword v28, v58, s[8:9]
	s_waitcnt vmcnt(1)
	v_readfirstlane_b32 s8, v26
	s_waitcnt vmcnt(0)
	v_readfirstlane_b32 s6, v28
	s_cmp_lg_u32 s6, 0
	v_readfirstlane_b32 s6, v27
	s_cbranch_scc1 .LBB0_2072
	s_add_u32 s0, s3, s0
	s_addc_u32 s1, s10, s1
	s_lshl_b64 s[22:23], s[4:5], 12
	v_lshl_add_u64 v[28:29], v[22:23], 0, s[22:23]
	global_load_dwordx2 v[26:27], v[28:29], off
	global_load_dwordx2 v[30:31], v[28:29], off offset:512
	global_load_dwordx2 v[32:33], v[28:29], off offset:1024
	s_ashr_i32 s9, s8, 31
	s_ashr_i32 s7, s6, 31
	s_lshl_b64 s[8:9], s[8:9], 12
	s_lshl_b64 s[6:7], s[6:7], 12
	v_lshl_add_u64 v[34:35], v[24:25], 0, s[8:9]
	v_lshl_add_u64 v[38:39], v[24:25], 0, s[6:7]
	global_load_dwordx2 v[36:37], v[34:35], off
	global_load_dwordx2 v[40:41], v[38:39], off
	global_load_dwordx2 v[42:43], v[34:35], off offset:512
	global_load_dwordx2 v[44:45], v[38:39], off offset:512
	global_load_dwordx2 v[46:47], v[34:35], off offset:1024
	global_load_dwordx2 v[48:49], v[38:39], off offset:1024
	global_load_dwordx2 v[56:57], v58, s[0:1]
	global_load_dwordx2 v[50:51], v[28:29], off offset:1536
	global_load_dwordx2 v[52:53], v[34:35], off offset:1536
	global_load_dwordx2 v[54:55], v[38:39], off offset:1536
	global_load_dwordx2 v[70:71], v[28:29], off offset:2048
	global_load_dwordx2 v[72:73], v[28:29], off offset:2560
	global_load_dwordx2 v[74:75], v[28:29], off offset:3072
	global_load_dwordx2 v[76:77], v[34:35], off offset:2048
	global_load_dwordx2 v[78:79], v[34:35], off offset:2560
	global_load_dwordx2 v[80:81], v[34:35], off offset:3072
	global_load_dwordx2 v[82:83], v[38:39], off offset:2048
	global_load_dwordx2 v[84:85], v[38:39], off offset:2560
	global_load_dwordx2 v[86:87], v[38:39], off offset:3072
	global_load_dwordx2 v[88:89], v[28:29], off offset:3584
	global_load_dwordx2 v[90:91], v[34:35], off offset:3584
	v_cmp_lt_i32_e32 vcc, v63, v62
	s_waitcnt vmcnt(19)
	v_lshlrev_b32_e32 v96, 16, v40
	s_waitcnt vmcnt(18)
	v_lshlrev_b32_e32 v98, 16, v42
	v_and_b32_e32 v99, 0xffff0000, v42
	v_lshlrev_b32_e32 v42, 16, v43
	v_and_b32_e32 v43, 0xffff0000, v43
	s_waitcnt vmcnt(16)
	v_lshlrev_b32_e32 v102, 16, v46
	v_and_b32_e32 v103, 0xffff0000, v46
	s_waitcnt vmcnt(14)
	v_pk_mul_f32 v[42:43], v[56:57], v[42:43] op_sel_hi:[0,1]
	v_pk_mul_f32 v[102:103], v[56:57], v[102:103] op_sel_hi:[0,1]
	v_and_b32_e32 v97, 0xffff0000, v40
	v_lshlrev_b32_e32 v28, 16, v26
	v_lshlrev_b32_e32 v34, 16, v30
	v_and_b32_e32 v35, 0xffff0000, v30
	v_lshlrev_b32_e32 v30, 16, v31
	v_and_b32_e32 v31, 0xffff0000, v31
	v_lshlrev_b32_e32 v92, 16, v32
	v_and_b32_e32 v93, 0xffff0000, v32
	v_pk_fma_f32 v[30:31], v[30:31], s[2:3], v[42:43] op_sel_hi:[1,0,1]
	v_pk_fma_f32 v[42:43], v[92:93], s[2:3], v[102:103] op_sel_hi:[1,0,1]
	global_load_dwordx2 v[92:93], v[38:39], off offset:3584
	v_lshlrev_b32_e32 v94, 16, v36
	v_and_b32_e32 v95, 0xffff0000, v36
	v_and_b32_e32 v29, 0xffff0000, v26
	v_lshlrev_b32_e32 v36, 16, v37
	v_and_b32_e32 v37, 0xffff0000, v37
	v_pk_mul_f32 v[94:95], v[56:57], v[94:95] op_sel_hi:[0,1]
	v_lshlrev_b32_e32 v26, 16, v27
	v_and_b32_e32 v27, 0xffff0000, v27
	v_lshlrev_b32_e32 v100, 16, v44
	v_and_b32_e32 v101, 0xffff0000, v44
	v_lshlrev_b32_e32 v44, 16, v45
	v_and_b32_e32 v45, 0xffff0000, v45
	v_lshlrev_b32_e32 v46, 16, v47
	v_and_b32_e32 v47, 0xffff0000, v47
	v_lshlrev_b32_e32 v104, 16, v48
	v_and_b32_e32 v105, 0xffff0000, v48
	v_pk_mul_f32 v[36:37], v[56:57], v[36:37] op_sel_hi:[0,1]
	v_pk_fma_f32 v[28:29], v[28:29], s[2:3], v[94:95] op_sel_hi:[1,0,1]
	v_lshlrev_b32_e32 v32, 16, v33
	v_and_b32_e32 v33, 0xffff0000, v33
	v_lshlrev_b32_e32 v40, 16, v41
	v_and_b32_e32 v41, 0xffff0000, v41
	v_pk_mul_f32 v[46:47], v[56:57], v[46:47] op_sel_hi:[0,1]
	v_pk_fma_f32 v[26:27], v[26:27], s[2:3], v[36:37] op_sel_hi:[1,0,1]
	v_pk_fma_f32 v[36:37], v[56:57], v[96:97], v[28:29] op_sel:[1,0,0]
	v_pk_fma_f32 v[30:31], v[56:57], v[44:45], v[30:31] op_sel:[1,0,0]
	v_pk_fma_f32 v[28:29], v[56:57], v[104:105], v[42:43] op_sel:[1,0,0]
	s_waitcnt vmcnt(13)
	v_lshlrev_b32_e32 v42, 16, v52
	v_and_b32_e32 v43, 0xffff0000, v52
	v_lshlrev_b32_e32 v44, 16, v53
	v_and_b32_e32 v45, 0xffff0000, v53
	v_lshlrev_b32_e32 v48, 16, v49
	v_and_b32_e32 v49, 0xffff0000, v49
	v_pk_fma_f32 v[46:47], v[32:33], s[2:3], v[46:47] op_sel_hi:[1,0,1]
	v_pk_fma_f32 v[32:33], v[56:57], v[40:41], v[26:27] op_sel:[1,0,0]
	v_lshlrev_b32_e32 v40, 16, v50
	v_and_b32_e32 v41, 0xffff0000, v50
	v_lshlrev_b32_e32 v38, 16, v51
	v_and_b32_e32 v39, 0xffff0000, v51
	v_pk_mul_f32 v[44:45], v[56:57], v[44:45] op_sel_hi:[0,1]
	v_pk_mul_f32 v[42:43], v[56:57], v[42:43] op_sel_hi:[0,1]
	v_pk_fma_f32 v[26:27], v[56:57], v[48:49], v[46:47] op_sel:[1,0,0]
	s_waitcnt vmcnt(12)
	v_lshlrev_b32_e32 v46, 16, v54
	v_and_b32_e32 v47, 0xffff0000, v54
	v_lshlrev_b32_e32 v48, 16, v55
	v_and_b32_e32 v49, 0xffff0000, v55
	v_pk_fma_f32 v[40:41], v[40:41], s[2:3], v[42:43] op_sel_hi:[1,0,1]
	v_pk_fma_f32 v[38:39], v[38:39], s[2:3], v[44:45] op_sel_hi:[1,0,1]
	v_pk_fma_f32 v[40:41], v[56:57], v[46:47], v[40:41] op_sel:[1,0,0]
	v_pk_fma_f32 v[38:39], v[56:57], v[48:49], v[38:39] op_sel:[1,0,0]
	s_waitcnt vmcnt(8)
	v_lshlrev_b32_e32 v46, 16, v76
	v_and_b32_e32 v47, 0xffff0000, v76
	v_lshlrev_b32_e32 v48, 16, v77
	v_and_b32_e32 v49, 0xffff0000, v77
	v_lshlrev_b32_e32 v42, 16, v70
	v_and_b32_e32 v43, 0xffff0000, v70
	v_lshlrev_b32_e32 v44, 16, v71
	v_and_b32_e32 v45, 0xffff0000, v71
	v_pk_mul_f32 v[48:49], v[56:57], v[48:49] op_sel_hi:[0,1]
	v_pk_mul_f32 v[46:47], v[56:57], v[46:47] op_sel_hi:[0,1]
	s_waitcnt vmcnt(5)
	v_lshlrev_b32_e32 v50, 16, v82
	v_and_b32_e32 v51, 0xffff0000, v82
	v_lshlrev_b32_e32 v52, 16, v83
	v_and_b32_e32 v53, 0xffff0000, v83
	v_pk_fma_f32 v[46:47], v[42:43], s[2:3], v[46:47] op_sel_hi:[1,0,1]
	v_pk_fma_f32 v[42:43], v[44:45], s[2:3], v[48:49] op_sel_hi:[1,0,1]
	v_pk_fma_f32 v[44:45], v[56:57], v[50:51], v[46:47] op_sel:[1,0,0]
	v_pk_fma_f32 v[42:43], v[56:57], v[52:53], v[42:43] op_sel:[1,0,0]
	v_lshlrev_b32_e32 v50, 16, v78
	v_and_b32_e32 v51, 0xffff0000, v78
	v_lshlrev_b32_e32 v52, 16, v79
	v_and_b32_e32 v53, 0xffff0000, v79
	v_lshlrev_b32_e32 v46, 16, v72
	v_and_b32_e32 v47, 0xffff0000, v72
	v_lshlrev_b32_e32 v48, 16, v73
	v_and_b32_e32 v49, 0xffff0000, v73
	v_pk_mul_f32 v[52:53], v[56:57], v[52:53] op_sel_hi:[0,1]
	v_pk_mul_f32 v[50:51], v[56:57], v[50:51] op_sel_hi:[0,1]
	s_waitcnt vmcnt(4)
	v_lshlrev_b32_e32 v54, 16, v84
	v_and_b32_e32 v55, 0xffff0000, v84
	v_lshlrev_b32_e32 v70, 16, v85
	v_and_b32_e32 v71, 0xffff0000, v85
	v_pk_fma_f32 v[50:51], v[46:47], s[2:3], v[50:51] op_sel_hi:[1,0,1]
	v_pk_fma_f32 v[46:47], v[48:49], s[2:3], v[52:53] op_sel_hi:[1,0,1]
	v_pk_fma_f32 v[48:49], v[56:57], v[54:55], v[50:51] op_sel:[1,0,0]
	v_pk_fma_f32 v[46:47], v[56:57], v[70:71], v[46:47] op_sel:[1,0,0]
	v_lshlrev_b32_e32 v54, 16, v80
	v_and_b32_e32 v55, 0xffff0000, v80
	v_lshlrev_b32_e32 v70, 16, v81
	v_and_b32_e32 v71, 0xffff0000, v81
	v_lshlrev_b32_e32 v50, 16, v74
	v_and_b32_e32 v51, 0xffff0000, v74
	v_lshlrev_b32_e32 v52, 16, v75
	v_and_b32_e32 v53, 0xffff0000, v75
	v_pk_mul_f32 v[70:71], v[56:57], v[70:71] op_sel_hi:[0,1]
	v_pk_mul_f32 v[54:55], v[56:57], v[54:55] op_sel_hi:[0,1]
	s_waitcnt vmcnt(3)
	v_lshlrev_b32_e32 v72, 16, v86
	v_and_b32_e32 v73, 0xffff0000, v86
	v_lshlrev_b32_e32 v74, 16, v87
	v_and_b32_e32 v75, 0xffff0000, v87
	v_pk_fma_f32 v[54:55], v[50:51], s[2:3], v[54:55] op_sel_hi:[1,0,1]
	v_pk_fma_f32 v[50:51], v[52:53], s[2:3], v[70:71] op_sel_hi:[1,0,1]
	v_pk_mul_f32 v[98:99], v[56:57], v[98:99] op_sel_hi:[0,1]
	v_pk_fma_f32 v[50:51], v[56:57], v[74:75], v[50:51] op_sel:[1,0,0]
	v_pk_fma_f32 v[52:53], v[56:57], v[72:73], v[54:55] op_sel:[1,0,0]
	s_waitcnt vmcnt(1)
	v_lshlrev_b32_e32 v72, 16, v90
	v_and_b32_e32 v73, 0xffff0000, v90
	v_lshlrev_b32_e32 v74, 16, v91
	v_and_b32_e32 v75, 0xffff0000, v91
	v_pk_fma_f32 v[34:35], v[34:35], s[2:3], v[98:99] op_sel_hi:[1,0,1]
	v_lshlrev_b32_e32 v54, 16, v88
	v_and_b32_e32 v55, 0xffff0000, v88
	v_lshlrev_b32_e32 v70, 16, v89
	v_and_b32_e32 v71, 0xffff0000, v89
	v_pk_mul_f32 v[74:75], v[56:57], v[74:75] op_sel_hi:[0,1]
	v_pk_mul_f32 v[72:73], v[56:57], v[72:73] op_sel_hi:[0,1]
	v_pk_fma_f32 v[34:35], v[56:57], v[100:101], v[34:35] op_sel:[1,0,0]
	s_waitcnt vmcnt(0)
	v_lshlrev_b32_e32 v76, 16, v92
	v_and_b32_e32 v77, 0xffff0000, v92
	v_lshlrev_b32_e32 v78, 16, v93
	v_and_b32_e32 v79, 0xffff0000, v93
	v_pk_fma_f32 v[72:73], v[54:55], s[2:3], v[72:73] op_sel_hi:[1,0,1]
	v_pk_fma_f32 v[54:55], v[70:71], s[2:3], v[74:75] op_sel_hi:[1,0,1]
	v_mov_b32_e32 v70, v36
	v_pk_fma_f32 v[54:55], v[56:57], v[78:79], v[54:55] op_sel:[1,0,0]
	v_pk_fma_f32 v[56:57], v[56:57], v[76:77], v[72:73] op_sel:[1,0,0]
	v_mov_b32_e32 v71, v34
	v_mov_b32_e32 v72, v37
	v_mov_b32_e32 v73, v35
	v_pk_add_f32 v[70:71], v[70:71], v[72:73]
	v_mov_b32_e32 v72, v32
	v_mov_b32_e32 v73, v30
	v_mov_b32_e32 v74, v33
	v_mov_b32_e32 v75, v31
	v_pk_add_f32 v[72:73], v[72:73], v[74:75]
	v_mov_b32_e32 v74, v28
	v_pk_add_f32 v[70:71], v[70:71], v[72:73]
	v_pk_mov_b32 v[72:73], v[28:29], v[26:27] op_sel:[1,0]
	v_mov_b32_e32 v75, v27
	v_pk_add_f32 v[72:73], v[72:73], v[74:75]
	v_add_f32_e32 v69, 0, v70
	v_pk_add_f32 v[72:73], v[72:73], v[72:73] op_sel:[0,1] op_sel_hi:[1,0]
	v_add_f32_e32 v70, v69, v71
	v_add_f32_e32 v74, v40, v41
	v_add_f32_e32 v76, v38, v39
	v_mov_b32_e32 v71, v44
	v_mov_b32_e32 v73, v45
	v_mov_b32_e32 v75, v42
	v_mov_b32_e32 v77, v43
	v_pk_add_f32 v[70:71], v[70:71], v[72:73]
	v_pk_add_f32 v[72:73], v[74:75], v[76:77]
	v_mov_b32_e32 v74, v48
	v_pk_add_f32 v[70:71], v[70:71], v[72:73]
	v_pk_mov_b32 v[72:73], v[48:49], v[46:47] op_sel:[1,0]
	v_mov_b32_e32 v75, v47
	v_pk_add_f32 v[72:73], v[72:73], v[74:75]
	v_pk_add_f32 v[70:71], v[70:71], v[70:71] op_sel:[0,1] op_sel_hi:[1,0]
	v_pk_add_f32 v[72:73], v[72:73], v[72:73] op_sel:[0,1] op_sel_hi:[1,0]
	v_add_f32_e32 v74, v52, v53
	v_add_f32_e32 v76, v50, v51
	v_mov_b32_e32 v71, v56
	v_mov_b32_e32 v73, v57
	v_mov_b32_e32 v75, v54
	v_mov_b32_e32 v77, v55
	v_pk_add_f32 v[70:71], v[70:71], v[72:73]
	v_pk_add_f32 v[72:73], v[74:75], v[76:77]
	s_nop 0
	v_pk_add_f32 v[70:71], v[70:71], v[72:73]
	s_nop 0
	v_add_f32_e32 v69, v70, v71
	v_cndmask_b32_e32 v70, v61, v63, vcc
	v_lshlrev_b32_e32 v78, 2, v70
	ds_bpermute_b32 v70, v78, v69
	v_cmp_lt_i32_e32 vcc, v64, v62
	s_waitcnt lgkmcnt(0)
	v_add_f32_e32 v69, v69, v70
	v_cndmask_b32_e32 v70, v61, v64, vcc
	v_lshlrev_b32_e32 v86, 2, v70
	ds_bpermute_b32 v70, v86, v69
	v_cmp_lt_i32_e32 vcc, v65, v62
	s_waitcnt lgkmcnt(0)
	v_add_f32_e32 v69, v69, v70
	v_cndmask_b32_e32 v70, v61, v65, vcc
	v_lshlrev_b32_e32 v102, 2, v70
	ds_bpermute_b32 v70, v102, v69
	v_cmp_lt_i32_e32 vcc, v66, v62
	s_waitcnt lgkmcnt(0)
	v_add_f32_e32 v69, v69, v70
	v_cndmask_b32_e32 v70, v61, v66, vcc
	v_lshlrev_b32_e32 v118, 2, v70
	ds_bpermute_b32 v70, v118, v69
	v_cmp_lt_i32_e32 vcc, v67, v62
	s_waitcnt lgkmcnt(0)
	v_add_f32_e32 v69, v69, v70
	v_cndmask_b32_e32 v70, v61, v67, vcc
	v_lshlrev_b32_e32 v134, 2, v70
	ds_bpermute_b32 v70, v134, v69
	v_cmp_lt_i32_e32 vcc, v68, v62
	s_waitcnt lgkmcnt(0)
	v_add_f32_e32 v69, v69, v70
	v_cndmask_b32_e32 v70, v61, v68, vcc
	v_lshlrev_b32_e32 v135, 2, v70
	ds_bpermute_b32 v70, v135, v69
	s_waitcnt lgkmcnt(0)
	v_add_f32_e32 v69, v69, v70
	v_fmamk_f32 v37, v69, 0xba000000, v37
	v_fmamk_f32 v35, v69, 0xba000000, v35
	v_fmamk_f32 v33, v69, 0xba000000, v33
	v_fmac_f32_e32 v36, 0xba000000, v69
	v_fmamk_f32 v31, v69, 0xba000000, v31
	v_fmac_f32_e32 v34, 0xba000000, v69
	v_mov_b32_e32 v72, v37
	v_mov_b32_e32 v73, v35
	v_fmac_f32_e32 v32, 0xba000000, v69
	v_fmac_f32_e32 v30, 0xba000000, v69
	v_mov_b32_e32 v70, v36
	v_mov_b32_e32 v71, v34
	v_pk_mul_f32 v[72:73], v[72:73], v[72:73]
	v_mov_b32_e32 v74, v33
	v_mov_b32_e32 v75, v31
	v_pk_fma_f32 v[70:71], v[70:71], v[70:71], v[72:73]
	v_mov_b32_e32 v72, v32
	v_mov_b32_e32 v73, v30
	v_pk_mul_f32 v[74:75], v[74:75], v[74:75]
	v_fmamk_f32 v29, v69, 0xba000000, v29
	v_pk_fma_f32 v[72:73], v[72:73], v[72:73], v[74:75]
	v_fmac_f32_e32 v28, 0xba000000, v69
	v_pk_add_f32 v[70:71], v[70:71], v[72:73]
	v_fmamk_f32 v27, v69, 0xba000000, v27
	v_fmac_f32_e32 v26, 0xba000000, v69
	v_pk_add_f32 v[70:71], v[70:71], v[70:71] op_sel_hi:[0,1]
	v_pk_mul_f32 v[72:73], v[26:27], v[26:27]
	v_pk_mul_f32 v[74:75], v[28:29], v[28:29]
	v_fmac_f32_e32 v40, 0xba000000, v69
	v_pk_mov_b32 v[76:77], v[74:75], v[72:73] op_sel:[1,0]
	v_mov_b32_e32 v75, v73
	v_fmamk_f32 v41, v69, 0xba000000, v41
	v_fmac_f32_e32 v38, 0xba000000, v69
	v_mul_f32_e32 v70, v40, v40
	v_pk_add_f32 v[72:73], v[76:77], v[74:75]
	v_fmamk_f32 v39, v69, 0xba000000, v39
	v_pk_fma_f32 v[74:75], v[40:41], v[40:41], v[70:71] op_sel_hi:[1,1,0]
	v_mul_f32_e32 v70, v38, v38
	v_pk_add_f32 v[72:73], v[72:73], v[72:73] op_sel_hi:[0,1]
	v_pk_fma_f32 v[76:77], v[38:39], v[38:39], v[70:71] op_sel_hi:[1,1,0]
	v_fmamk_f32 v43, v69, 0xba000000, v43
	v_fmac_f32_e32 v42, 0xba000000, v69
	v_fmamk_f32 v45, v69, 0xba000000, v45
	v_fmac_f32_e32 v44, 0xba000000, v69
	v_mul_f32_e32 v74, v44, v44
	v_mul_f32_e32 v76, v45, v45
	v_mul_f32_e32 v72, v42, v42
	v_mul_f32_e32 v70, v43, v43
	v_pk_add_f32 v[74:75], v[74:75], v[76:77]
	v_pk_add_f32 v[70:71], v[72:73], v[70:71]
	v_fmamk_f32 v49, v69, 0xba000000, v49
	v_pk_add_f32 v[70:71], v[74:75], v[70:71]
	v_fmac_f32_e32 v48, 0xba000000, v69
	v_fmamk_f32 v47, v69, 0xba000000, v47
	v_fmac_f32_e32 v46, 0xba000000, v69
	v_pk_add_f32 v[70:71], v[70:71], v[70:71] op_sel_hi:[0,1]
	v_pk_mul_f32 v[72:73], v[46:47], v[46:47]
	v_pk_mul_f32 v[74:75], v[48:49], v[48:49]
	v_fmac_f32_e32 v52, 0xba000000, v69
	v_pk_mov_b32 v[76:77], v[74:75], v[72:73] op_sel:[1,0]
	v_mov_b32_e32 v75, v73
	v_fmamk_f32 v53, v69, 0xba000000, v53
	v_fmac_f32_e32 v50, 0xba000000, v69
	v_mul_f32_e32 v70, v52, v52
	v_pk_add_f32 v[72:73], v[76:77], v[74:75]
	v_fmamk_f32 v51, v69, 0xba000000, v51
	v_pk_fma_f32 v[74:75], v[52:53], v[52:53], v[70:71] op_sel_hi:[1,1,0]
	v_mul_f32_e32 v70, v50, v50
	v_pk_add_f32 v[72:73], v[72:73], v[72:73] op_sel_hi:[0,1]
	v_pk_fma_f32 v[76:77], v[50:51], v[50:51], v[70:71] op_sel_hi:[1,1,0]
	v_fmamk_f32 v55, v69, 0xba000000, v55
	v_fmac_f32_e32 v54, 0xba000000, v69
	v_fmamk_f32 v57, v69, 0xba000000, v57
	v_fmac_f32_e32 v56, 0xba000000, v69
	v_mul_f32_e32 v74, v56, v56
	v_mul_f32_e32 v76, v57, v57
	v_mul_f32_e32 v72, v54, v54
	v_mul_f32_e32 v70, v55, v55
	v_pk_add_f32 v[74:75], v[74:75], v[76:77]
	v_pk_add_f32 v[70:71], v[72:73], v[70:71]
	s_nop 0
	v_pk_add_f32 v[70:71], v[74:75], v[70:71]
	s_nop 0
	v_add_f32_e32 v69, v70, v71
	ds_bpermute_b32 v78, v78, v69
	global_load_dwordx4 v[70:73], v[2:3], off
	global_load_dwordx4 v[74:77], v[4:5], off
	s_waitcnt lgkmcnt(0)
	v_add_f32_e32 v69, v69, v78
	ds_bpermute_b32 v94, v86, v69
	global_load_dwordx4 v[78:81], v[2:3], off offset:1024
	global_load_dwordx4 v[82:85], v[4:5], off offset:1024
	global_load_dwordx4 v[86:89], v[2:3], off offset:2048
	global_load_dwordx4 v[90:93], v[4:5], off offset:2048
	s_waitcnt lgkmcnt(0)
	v_add_f32_e32 v69, v69, v94
	ds_bpermute_b32 v110, v102, v69
	global_load_dwordx4 v[94:97], v[2:3], off offset:3072
	global_load_dwordx4 v[98:101], v[4:5], off offset:3072
	global_load_dwordx4 v[102:105], v[6:7], off
	global_load_dwordx4 v[106:109], v[8:9], off
	s_waitcnt lgkmcnt(0)
	v_add_f32_e32 v69, v69, v110
	ds_bpermute_b32 v126, v118, v69
	global_load_dwordx4 v[110:113], v[10:11], off
	global_load_dwordx4 v[114:117], v[12:13], off
	global_load_dwordx4 v[118:121], v[14:15], off
	global_load_dwordx4 v[122:125], v[16:17], off
	s_waitcnt lgkmcnt(0)
	v_add_f32_e32 v69, v69, v126
	global_load_dwordx4 v[126:129], v[18:19], off
	global_load_dwordx4 v[130:133], v[20:21], off
	ds_bpermute_b32 v134, v134, v69
	s_waitcnt lgkmcnt(0)
	v_add_f32_e32 v69, v69, v134
	ds_bpermute_b32 v134, v135, v69
	s_waitcnt lgkmcnt(0)
	v_add_f32_e32 v69, v69, v134
	v_fmamk_f32 v69, v69, 0x3a000000, v59
	v_mul_f32_e32 v134, 0x4f800000, v69
	v_cmp_gt_f32_e32 vcc, s21, v69
	s_nop 1
	v_cndmask_b32_e32 v69, v69, v134, vcc
	v_sqrt_f32_e32 v134, v69
	s_nop 0
	v_add_u32_e32 v135, -1, v134
	v_fma_f32 v136, -v135, v134, v69
	v_cmp_ge_f32_e64 s[0:1], 0, v136
	v_add_u32_e32 v136, 1, v134
	s_nop 0
	v_cndmask_b32_e64 v135, v134, v135, s[0:1]
	v_fma_f32 v134, -v136, v134, v69
	v_cmp_lt_f32_e64 s[0:1], 0, v134
	s_nop 1
	v_cndmask_b32_e64 v134, v135, v136, s[0:1]
	v_mul_f32_e32 v135, 0x37800000, v134
	v_cndmask_b32_e32 v134, v134, v135, vcc
	v_cmp_class_f32_e32 vcc, v69, v60
	s_nop 1
	v_cndmask_b32_e32 v69, v134, v69, vcc
	v_div_scale_f32 v134, s[0:1], v69, v69, 1.0
	v_rcp_f32_e32 v135, v134
	s_lshl_b64 s[0:1], s[4:5], 13
	s_add_u32 s0, s64, s0
	s_addc_u32 s1, s65, s1
	v_fma_f32 v136, -v134, v135, 1.0
	v_fmac_f32_e32 v135, v136, v135
	v_div_scale_f32 v136, vcc, 1.0, v69, 1.0
	v_mul_f32_e32 v137, v136, v135
	v_fma_f32 v138, -v134, v137, v136
	v_fmac_f32_e32 v137, v138, v135
	v_fma_f32 v134, -v134, v137, v136
	v_div_fmas_f32 v134, v134, v135, v137
	v_div_fixup_f32 v134, v134, v69, 1.0
	v_pk_mul_f32 v[32:33], v[32:33], v[134:135] op_sel_hi:[1,0]
	v_pk_mul_f32 v[34:35], v[34:35], v[134:135] op_sel_hi:[1,0]
	v_pk_mul_f32 v[30:31], v[30:31], v[134:135] op_sel_hi:[1,0]
	v_pk_mul_f32 v[36:37], v[36:37], v[134:135] op_sel_hi:[1,0]
	s_waitcnt vmcnt(14)
	v_pk_fma_f32 v[72:73], v[72:73], v[32:33], v[76:77]
	v_pk_mul_f32 v[26:27], v[26:27], v[134:135] op_sel_hi:[1,0]
	v_pk_fma_f32 v[70:71], v[70:71], v[36:37], v[74:75]
	s_waitcnt vmcnt(12)
	v_pk_fma_f32 v[32:33], v[80:81], v[30:31], v[84:85]
	v_pk_fma_f32 v[30:31], v[78:79], v[34:35], v[82:83]
	v_pk_mul_f32 v[34:35], v[28:29], v[134:135] op_sel_hi:[1,0]
	s_waitcnt vmcnt(10)
	v_pk_fma_f32 v[28:29], v[88:89], v[26:27], v[92:93]
	v_pk_fma_f32 v[26:27], v[86:87], v[34:35], v[90:91]
	v_pk_mul_f32 v[34:35], v[40:41], v[134:135] op_sel_hi:[1,0]
	v_pk_mul_f32 v[36:37], v[38:39], v[134:135] op_sel_hi:[1,0]
	v_pk_mul_f32 v[38:39], v[44:45], v[134:135] op_sel_hi:[1,0]
	v_pk_mul_f32 v[44:45], v[46:47], v[134:135] op_sel_hi:[1,0]
	v_pk_mul_f32 v[46:47], v[52:53], v[134:135] op_sel_hi:[1,0]
	v_pk_mul_f32 v[52:53], v[54:55], v[134:135] op_sel_hi:[1,0]
	v_lshl_add_u64 v[54:55], v[0:1], 2, s[0:1]
	s_waitcnt vmcnt(8)
	v_pk_fma_f32 v[36:37], v[96:97], v[36:37], v[100:101]
	v_pk_fma_f32 v[34:35], v[94:95], v[34:35], v[98:99]
	v_pk_mul_f32 v[40:41], v[42:43], v[134:135] op_sel_hi:[1,0]
	global_store_dwordx4 v[54:55], v[70:73], off sc1
	global_store_dwordx4 v[54:55], v[30:33], off offset:1024 sc1
	global_store_dwordx4 v[54:55], v[26:29], off offset:2048 sc1
	global_store_dwordx4 v[54:55], v[34:37], off offset:3072 sc1
	s_waitcnt vmcnt(10)
	v_pk_fma_f32 v[40:41], v[104:105], v[40:41], v[108:109]
	v_add_co_u32_e32 v26, vcc, 0x1000, v54
	v_pk_fma_f32 v[38:39], v[102:103], v[38:39], v[106:107]
	v_pk_mul_f32 v[42:43], v[48:49], v[134:135] op_sel_hi:[1,0]
	v_pk_mul_f32 v[48:49], v[50:51], v[134:135] op_sel_hi:[1,0]
	v_pk_mul_f32 v[50:51], v[56:57], v[134:135] op_sel_hi:[1,0]
	v_addc_co_u32_e32 v27, vcc, 0, v55, vcc
	s_waitcnt vmcnt(8)
	v_pk_fma_f32 v[44:45], v[112:113], v[44:45], v[116:117]
	v_pk_fma_f32 v[42:43], v[110:111], v[42:43], v[114:115]
	s_waitcnt vmcnt(6)
	v_pk_fma_f32 v[48:49], v[120:121], v[48:49], v[124:125]
	v_pk_fma_f32 v[46:47], v[118:119], v[46:47], v[122:123]
	s_waitcnt vmcnt(4)
	v_pk_fma_f32 v[52:53], v[128:129], v[52:53], v[132:133]
	v_pk_fma_f32 v[50:51], v[126:127], v[50:51], v[130:131]
	global_store_dwordx4 v[26:27], v[38:41], off sc1
	global_store_dwordx4 v[26:27], v[42:45], off offset:1024 sc1
	global_store_dwordx4 v[26:27], v[46:49], off offset:2048 sc1
	global_store_dwordx4 v[26:27], v[50:53], off offset:3072 sc1
	s_branch .LBB0_2072
